# speedup vs baseline: 1.0112x; 1.0001x over previous
.LBB12_5:
	v_lshlrev_b32_e32 v0, 2, v0
	v_and_b32_e32 v58, 0xfc, v0
	v_lshlrev_b64 v[4:5], 11, v[4:5]
	v_lshlrev_b32_e32 v0, 2, v58
	v_mov_b32_e32 v1, 0
	s_waitcnt lgkmcnt(0)
	v_lshl_add_u64 v[4:5], s[24:25], 0, v[4:5]
	v_lshl_add_u64 v[4:5], v[4:5], 0, v[0:1]
	global_load_dwordx4 v[8:11], v[4:5], off
	global_load_dwordx4 v[12:15], v0, s[20:21]
	global_load_dwordx4 v[16:19], v0, s[20:21] offset:1024
	global_load_dwordx4 v[20:23], v[4:5], off offset:1024
	v_lshlrev_b64 v[4:5], 11, v[2:3]
	v_lshl_add_u64 v[24:25], s[22:23], 0, v[4:5]
	v_lshl_add_u64 v[40:41], v[24:25], 0, v[0:1]
	global_load_dwordx4 v[24:27], v[40:41], off
	global_load_dwordx4 v[28:31], v[40:41], off offset:1024
	global_load_dwordx4 v[32:35], v0, s[12:13]
	global_load_dwordx4 v[36:39], v0, s[12:13] offset:1024
	v_lshlrev_b64 v[6:7], 11, v[6:7]
	v_lshl_add_u64 v[6:7], s[18:19], 0, v[6:7]
	v_lshl_add_u64 v[52:53], v[6:7], 0, v[0:1]
	global_load_dwordx4 v[40:43], v0, s[14:15]
	global_load_dwordx4 v[44:47], v0, s[8:9]
	global_load_dwordx4 v[48:51], v0, s[10:11]
	v_mov_b32_e32 v59, 0x3727c5ac
	s_mov_b32 s12, 0xf800000
	v_mov_b32_e32 v60, 0x260
	v_lshl_add_u64 v[4:5], s[4:5], 0, v[4:5]
	v_lshlrev_b64 v[2:3], 10, v[2:3]
	s_waitcnt vmcnt(9)
	v_pk_add_f32 v[54:55], v[12:13], v[8:9]
	global_load_dwordx4 v[6:9], v0, s[14:15] offset:1024
	s_waitcnt vmcnt(8)
	v_pk_add_f32 v[20:21], v[16:17], v[20:21]
	v_pk_add_f32 v[18:19], v[18:19], v[22:23]
	v_pk_add_f32 v[56:57], v[14:15], v[10:11]
	global_load_dwordx4 v[10:13], v0, s[8:9] offset:1024
	global_load_dwordx4 v[14:17], v0, s[10:11] offset:1024
	s_waitcnt vmcnt(9)
	v_pk_add_f32 v[54:55], v[24:25], v[54:55]
	s_waitcnt vmcnt(8)
	v_pk_add_f32 v[28:29], v[28:29], v[20:21]
	v_pk_add_f32 v[30:31], v[30:31], v[18:19]
	global_load_dwordx4 v[18:21], v[52:53], off
	global_load_dwordx4 v[22:25], v[52:53], off offset:1024
	v_add_f32_e32 v52, 0, v54
	v_pk_add_f32 v[26:27], v[26:27], v[56:57]
	v_add_f32_e32 v52, v52, v55
	v_add_f32_e32 v52, v52, v26
	v_add_f32_e32 v52, v52, v27
	v_add_f32_e32 v52, v52, v28
	v_add_f32_e32 v52, v52, v29
	v_add_f32_e32 v52, v52, v30
	v_add_f32_e32 v52, v52, v31
	s_nop 1
	v_add_f32_dpp v52, v52, v52 quad_perm:[1,0,3,2] row_mask:0xf bank_mask:0xf bound_ctrl:1
	s_nop 1
	v_add_f32_dpp v52, v52, v52 quad_perm:[2,3,0,1] row_mask:0xf bank_mask:0xf bound_ctrl:1
	s_nop 1
	v_add_f32_dpp v52, v52, v52 row_half_mirror row_mask:0xf bank_mask:0xf bound_ctrl:1
	s_nop 1
	v_add_f32_dpp v52, v52, v52 row_mirror row_mask:0xf bank_mask:0xf bound_ctrl:1
	s_nop 0
	v_readlane_b32 s8, v52, 16
	v_readlane_b32 s9, v52, 48
	v_readlane_b32 s0, v52, 0
	v_readlane_b32 s1, v52, 32
	v_mov_b32_e32 v52, s8
	v_mov_b32_e32 v53, s9
	v_pk_add_f32 v[52:53], s[0:1], v[52:53]
	s_nop 0
	v_add_f32_e32 v52, v52, v53
	v_mul_f32_e32 v52, 0x3b000000, v52
	v_pk_add_f32 v[54:55], v[54:55], v[52:53] op_sel_hi:[1,0] neg_lo:[0,1] neg_hi:[0,1]
	v_pk_add_f32 v[26:27], v[26:27], v[52:53] op_sel_hi:[1,0] neg_lo:[0,1] neg_hi:[0,1]
	v_pk_add_f32 v[28:29], v[28:29], v[52:53] op_sel_hi:[1,0] neg_lo:[0,1] neg_hi:[0,1]
	v_pk_add_f32 v[30:31], v[30:31], v[52:53] op_sel_hi:[1,0] neg_lo:[0,1] neg_hi:[0,1]
	v_pk_mul_f32 v[52:53], v[54:55], v[54:55]
	s_waitcnt vmcnt(9)
	v_pk_mul_f32 v[32:33], v[32:33], v[54:55]
	v_add_f32_e32 v56, v52, v53
	v_pk_mul_f32 v[52:53], v[26:27], v[26:27]
	v_pk_mul_f32 v[26:27], v[34:35], v[26:27]
	v_add_f32_e32 v52, v56, v52
	v_add_f32_e32 v56, v52, v53
	v_pk_mul_f32 v[52:53], v[28:29], v[28:29]
	s_waitcnt vmcnt(8)
	v_pk_mul_f32 v[28:29], v[36:37], v[28:29]
	v_add_f32_e32 v52, v56, v52
	v_add_f32_e32 v56, v52, v53
	v_pk_mul_f32 v[52:53], v[30:31], v[30:31]
	v_pk_mul_f32 v[30:31], v[38:39], v[30:31]
	v_add_f32_e32 v52, v56, v52
	v_add_f32_e32 v52, v52, v53
	s_nop 1
	v_add_f32_dpp v52, v52, v52 quad_perm:[1,0,3,2] row_mask:0xf bank_mask:0xf bound_ctrl:1
	s_nop 1
	v_add_f32_dpp v52, v52, v52 quad_perm:[2,3,0,1] row_mask:0xf bank_mask:0xf bound_ctrl:1
	s_nop 1
	v_add_f32_dpp v52, v52, v52 row_half_mirror row_mask:0xf bank_mask:0xf bound_ctrl:1
	s_nop 1
	v_add_f32_dpp v52, v52, v52 row_mirror row_mask:0xf bank_mask:0xf bound_ctrl:1
	s_nop 0
	v_readlane_b32 s8, v52, 16
	v_readlane_b32 s9, v52, 48
	v_readlane_b32 s0, v52, 0
	v_readlane_b32 s1, v52, 32
	v_mov_b32_e32 v52, s8
	v_mov_b32_e32 v53, s9
	v_pk_add_f32 v[52:53], s[0:1], v[52:53]
	s_nop 0
	v_add_f32_e32 v52, v52, v53
	v_fmamk_f32 v52, v52, 0x3b000000, v59
	v_mul_f32_e32 v53, 0x4f800000, v52
	v_cmp_gt_f32_e32 vcc, s12, v52
	s_nop 1
	v_cndmask_b32_e32 v52, v52, v53, vcc
	v_sqrt_f32_e32 v53, v52
	s_nop 0
	v_add_u32_e32 v34, -1, v53
	v_add_u32_e32 v35, 1, v53
	v_fma_f32 v36, -v34, v53, v52
	v_fma_f32 v37, -v35, v53, v52
	v_cmp_ge_f32_e64 s[0:1], 0, v36
	s_nop 1
	v_cndmask_b32_e64 v34, v53, v34, s[0:1]
	v_cmp_lt_f32_e64 s[0:1], 0, v37
	s_nop 1
	v_cndmask_b32_e64 v34, v34, v35, s[0:1]
	v_mul_f32_e32 v35, 0x37800000, v34
	v_cndmask_b32_e32 v34, v34, v35, vcc
	v_cmp_class_f32_e32 vcc, v52, v60
	s_nop 1
	v_cndmask_b32_e32 v34, v34, v52, vcc
	v_div_scale_f32 v35, s[0:1], v34, v34, 1.0
	v_rcp_f32_e32 v36, v35
	v_div_scale_f32 v37, vcc, 1.0, v34, 1.0
	v_fma_f32 v38, -v35, v36, 1.0
	v_fmac_f32_e32 v36, v38, v36
	v_mul_f32_e32 v38, v37, v36
	v_fma_f32 v39, -v35, v38, v37
	v_fmac_f32_e32 v38, v39, v36
	v_fma_f32 v35, -v35, v38, v37
	v_div_fmas_f32 v35, v35, v36, v38
	v_div_fixup_f32 v34, v35, v34, 1.0
	s_waitcnt vmcnt(7)
	v_pk_fma_f32 v[32:33], v[34:35], v[32:33], v[40:41] op_sel_hi:[0,1,1]
	s_waitcnt vmcnt(4)
	v_pk_fma_f32 v[6:7], v[34:35], v[28:29], v[6:7] op_sel_hi:[0,1,1]
	s_waitcnt vmcnt(1)
	v_pk_add_f32 v[18:19], v[32:33], v[18:19]
	v_pk_fma_f32 v[26:27], v[34:35], v[26:27], v[42:43] op_sel_hi:[0,1,1]
	s_waitcnt vmcnt(0)
	v_pk_add_f32 v[6:7], v[6:7], v[22:23]
	v_add_f32_e32 v22, 0, v18
	v_pk_add_f32 v[20:21], v[26:27], v[20:21]
	v_add_f32_e32 v22, v22, v19
	v_add_f32_e32 v22, v22, v20
	v_add_f32_e32 v22, v22, v21
	v_pk_fma_f32 v[8:9], v[34:35], v[30:31], v[8:9] op_sel_hi:[0,1,1]
	v_add_f32_e32 v22, v22, v6
	v_pk_add_f32 v[8:9], v[8:9], v[24:25]
	v_add_f32_e32 v22, v22, v7
	v_add_f32_e32 v22, v22, v8
	v_add_f32_e32 v22, v22, v9
	s_nop 1
	v_add_f32_dpp v22, v22, v22 quad_perm:[1,0,3,2] row_mask:0xf bank_mask:0xf bound_ctrl:1
	s_nop 1
	v_add_f32_dpp v22, v22, v22 quad_perm:[2,3,0,1] row_mask:0xf bank_mask:0xf bound_ctrl:1
	s_nop 1
	v_add_f32_dpp v22, v22, v22 row_half_mirror row_mask:0xf bank_mask:0xf bound_ctrl:1
	s_nop 1
	v_add_f32_dpp v22, v22, v22 row_mirror row_mask:0xf bank_mask:0xf bound_ctrl:1
	s_nop 0
	v_readlane_b32 s8, v22, 16
	v_readlane_b32 s9, v22, 48
	v_readlane_b32 s0, v22, 0
	v_readlane_b32 s1, v22, 32
	v_mov_b32_e32 v22, s8
	v_mov_b32_e32 v23, s9
	v_pk_add_f32 v[22:23], s[0:1], v[22:23]
	s_nop 0
	v_add_f32_e32 v22, v22, v23
	v_mul_f32_e32 v22, 0x3b000000, v22
	v_pk_add_f32 v[18:19], v[18:19], v[22:23] op_sel_hi:[1,0] neg_lo:[0,1] neg_hi:[0,1]
	v_pk_add_f32 v[20:21], v[20:21], v[22:23] op_sel_hi:[1,0] neg_lo:[0,1] neg_hi:[0,1]
	v_pk_add_f32 v[24:25], v[6:7], v[22:23] op_sel_hi:[1,0] neg_lo:[0,1] neg_hi:[0,1]
	v_pk_mul_f32 v[6:7], v[18:19], v[18:19]
	v_pk_add_f32 v[22:23], v[8:9], v[22:23] op_sel_hi:[1,0] neg_lo:[0,1] neg_hi:[0,1]
	v_pk_mul_f32 v[8:9], v[20:21], v[20:21]
	v_add_f32_e32 v6, v6, v7
	v_add_f32_e32 v6, v6, v8
	v_pk_mul_f32 v[26:27], v[24:25], v[24:25]
	v_add_f32_e32 v6, v6, v9
	v_add_f32_e32 v6, v6, v26
	v_pk_mul_f32 v[28:29], v[22:23], v[22:23]
	v_add_f32_e32 v6, v6, v27
	v_add_f32_e32 v6, v6, v28
	v_add_f32_e32 v6, v6, v29
	s_nop 1
	v_add_f32_dpp v6, v6, v6 quad_perm:[1,0,3,2] row_mask:0xf bank_mask:0xf bound_ctrl:1
	s_nop 1
	v_add_f32_dpp v6, v6, v6 quad_perm:[2,3,0,1] row_mask:0xf bank_mask:0xf bound_ctrl:1
	s_nop 1
	v_add_f32_dpp v6, v6, v6 row_half_mirror row_mask:0xf bank_mask:0xf bound_ctrl:1
	s_nop 1
	v_add_f32_dpp v6, v6, v6 row_mirror row_mask:0xf bank_mask:0xf bound_ctrl:1
	s_nop 0
	v_readlane_b32 s8, v6, 16
	v_readlane_b32 s9, v6, 48
	v_readlane_b32 s0, v6, 0
	v_readlane_b32 s1, v6, 32
	v_mov_b32_e32 v6, s8
	v_mov_b32_e32 v7, s9
	v_pk_add_f32 v[6:7], s[0:1], v[6:7]
	s_nop 0
	v_add_f32_e32 v6, v6, v7
	v_fmac_f32_e32 v59, 0x3b000000, v6
	v_mul_f32_e32 v6, 0x4f800000, v59
	v_cmp_gt_f32_e32 vcc, s12, v59
	s_nop 1
	v_cndmask_b32_e32 v6, v59, v6, vcc
	v_sqrt_f32_e32 v7, v6
	s_nop 0
	v_add_u32_e32 v8, -1, v7
	v_add_u32_e32 v9, 1, v7
	v_fma_f32 v26, -v8, v7, v6
	v_fma_f32 v27, -v9, v7, v6
	v_cmp_ge_f32_e64 s[0:1], 0, v26
	s_nop 1
	v_cndmask_b32_e64 v7, v7, v8, s[0:1]
	v_cmp_lt_f32_e64 s[0:1], 0, v27
	v_lshl_add_u64 v[26:27], v[4:5], 0, v[0:1]
	s_nop 0
	v_cndmask_b32_e64 v7, v7, v9, s[0:1]
	v_mul_f32_e32 v8, 0x37800000, v7
	v_cndmask_b32_e32 v7, v7, v8, vcc
	v_cmp_class_f32_e32 vcc, v6, v60
	s_nop 1
	v_cndmask_b32_e32 v6, v7, v6, vcc
	v_div_scale_f32 v7, s[0:1], v6, v6, 1.0
	v_rcp_f32_e32 v8, v7
	s_mov_b32 s0, 0x43000000
	v_fma_f32 v0, -v7, v8, 1.0
	v_fmac_f32_e32 v8, v0, v8
	v_div_scale_f32 v0, vcc, 1.0, v6, 1.0
	v_mul_f32_e32 v4, v0, v8
	v_fma_f32 v5, -v7, v4, v0
	v_fmac_f32_e32 v4, v5, v8
	v_fma_f32 v0, -v7, v4, v0
	v_div_fmas_f32 v0, v0, v8, v4
	v_div_fixup_f32 v0, v0, v6, 1.0
	v_pk_mul_f32 v[4:5], v[44:45], v[18:19]
	v_pk_mul_f32 v[6:7], v[46:47], v[20:21]
	v_pk_fma_f32 v[4:5], v[0:1], v[4:5], v[48:49] op_sel_hi:[0,1,1]
	v_pk_mul_f32 v[8:9], v[10:11], v[24:25]
	v_pk_fma_f32 v[6:7], v[0:1], v[6:7], v[50:51] op_sel_hi:[0,1,1]
	v_pk_fma_f32 v[8:9], v[0:1], v[8:9], v[14:15] op_sel_hi:[0,1,1]
	v_pk_mul_f32 v[10:11], v[12:13], v[22:23]
	v_fma_mixlo_f16 v12, v4, s0, 0
	v_pk_fma_f32 v[10:11], v[0:1], v[10:11], v[16:17] op_sel_hi:[0,1,1]
	global_store_dwordx4 v[26:27], v[4:7], off sc1
	global_store_dwordx4 v[26:27], v[8:11], off offset:1024 sc1
	v_mul_f32_e32 v0, 0x43000000, v4
	v_fma_mixlo_f16 v4, v4, s0, -v12 op_sel_hi:[0,0,1]
	v_fma_mixlo_f16 v12, v8, s0, 0
	v_mul_f32_e32 v13, 0x43000000, v8
	v_fma_mixlo_f16 v8, v8, s0, -v12 op_sel_hi:[0,0,1]
	v_mul_f32_e32 v12, 0x43000000, v5
	v_fma_mixlo_f16 v14, v5, s0, 0
	v_cvt_pk_f16_f32 v12, v0, v12
	v_mul_f32_e32 v0, 0x43000000, v9
	v_pk_mul_f32 v[16:17], v[6:7], s[0:1] op_sel_hi:[1,0]
	v_fma_mixhi_f16 v4, v5, s0, -v14 op_sel_hi:[0,0,1]
	v_cvt_pk_f16_f32 v14, v13, v0
	v_cvt_pk_f16_f32 v13, v16, v17
	v_pk_mul_f32 v[18:19], v[10:11], s[0:1] op_sel_hi:[1,0]
	v_cvt_f32_f16_e32 v16, v13
	v_cvt_f32_f16_sdwa v17, v13 dst_sel:DWORD dst_unused:UNUSED_PAD src0_sel:WORD_1
	v_cvt_pk_f16_f32 v15, v18, v19
	v_cvt_f32_f16_e32 v18, v15
	v_cvt_f32_f16_sdwa v19, v15 dst_sel:DWORD dst_unused:UNUSED_PAD src0_sel:WORD_1
	v_fma_mixlo_f16 v5, v9, s0, 0
	v_pk_fma_f32 v[6:7], v[6:7], s[0:1], v[16:17] op_sel_hi:[1,0,1] neg_lo:[0,0,1] neg_hi:[0,0,1]
	v_fma_mixhi_f16 v8, v9, s0, -v5 op_sel_hi:[0,0,1]
	v_cvt_pk_f16_f32 v5, v6, v7
	v_pk_fma_f32 v[6:7], v[10:11], s[0:1], v[18:19] op_sel_hi:[1,0,1] neg_lo:[0,0,1] neg_hi:[0,0,1]
	v_lshlrev_b32_e32 v0, 1, v58
	v_cvt_pk_f16_f32 v9, v6, v7
	v_lshl_add_u64 v[6:7], s[6:7], 0, v[2:3]
	v_lshl_add_u64 v[2:3], s[2:3], 0, v[2:3]
	v_lshl_add_u64 v[6:7], v[6:7], 0, v[0:1]
	v_lshl_add_u64 v[0:1], v[2:3], 0, v[0:1]
	v_mbcnt_lo_u32_b32 v20, -1, 0
	v_mbcnt_hi_u32_b32 v20, -1, v20
	v_and_b32_e32 v20, 1, v20
	v_cmp_eq_u32_e32 vcc, 1, v20
	v_mul_u32_u24_e32 v22, 0x1f8, v20
	v_mov_b32_e32 v23, 0
	s_nop 1
	v_mov_b32_dpp v24, v12 quad_perm:[1,0,3,2] row_mask:0xf bank_mask:0xf
	v_mov_b32_dpp v25, v13 quad_perm:[1,0,3,2] row_mask:0xf bank_mask:0xf
	v_mov_b32_dpp v26, v14 quad_perm:[1,0,3,2] row_mask:0xf bank_mask:0xf
	v_mov_b32_dpp v27, v15 quad_perm:[1,0,3,2] row_mask:0xf bank_mask:0xf
	s_nop 1
	v_cndmask_b32_e32 v28, v12, v26, vcc
	v_cndmask_b32_e32 v29, v13, v27, vcc
	v_cndmask_b32_e32 v30, v24, v14, vcc
	v_cndmask_b32_e32 v31, v25, v15, vcc
	v_lshl_add_u64 v[32:33], v[6:7], 0, v[22:23]
	global_store_dwordx4 v[32:33], v[28:31], off sc1
	s_nop 1
	v_mov_b32_dpp v24, v4 quad_perm:[1,0,3,2] row_mask:0xf bank_mask:0xf
	v_mov_b32_dpp v25, v5 quad_perm:[1,0,3,2] row_mask:0xf bank_mask:0xf
	v_mov_b32_dpp v26, v8 quad_perm:[1,0,3,2] row_mask:0xf bank_mask:0xf
	v_mov_b32_dpp v27, v9 quad_perm:[1,0,3,2] row_mask:0xf bank_mask:0xf
	s_nop 1
	v_cndmask_b32_e32 v28, v4, v26, vcc
	v_cndmask_b32_e32 v29, v5, v27, vcc
	v_cndmask_b32_e32 v30, v24, v8, vcc
	v_cndmask_b32_e32 v31, v25, v9, vcc
	v_lshl_add_u64 v[32:33], v[0:1], 0, v[22:23]
	global_store_dwordx4 v[32:33], v[28:31], off sc1
	s_nop 1
	s_endpgm
	s_endpgm
	s_endpgm
	s_endpgm
	s_endpgm
	s_endpgm
	s_endpgm
	s_endpgm

.LBB13_5:
	v_lshlrev_b32_e32 v0, 2, v0
	v_and_b32_e32 v58, 0xfc, v0
	v_lshlrev_b64 v[4:5], 11, v[4:5]
	s_load_dwordx2 s[0:1], s[0:1], 0x8
	v_lshlrev_b32_e32 v0, 2, v58
	v_mov_b32_e32 v1, 0
	s_waitcnt lgkmcnt(0)
	v_lshl_add_u64 v[4:5], s[24:25], 0, v[4:5]
	v_lshl_add_u64 v[4:5], v[4:5], 0, v[0:1]
	global_load_dwordx4 v[8:11], v[4:5], off
	global_load_dwordx4 v[12:15], v0, s[20:21]
	global_load_dwordx4 v[16:19], v0, s[20:21] offset:1024
	global_load_dwordx4 v[20:23], v[4:5], off offset:1024
	v_lshlrev_b64 v[4:5], 11, v[2:3]
	v_lshl_add_u64 v[32:33], s[22:23], 0, v[4:5]
	v_lshl_add_u64 v[34:35], v[32:33], 0, v[0:1]
	v_lshl_add_u64 v[32:33], s[0:1], 2, v[32:33]
	global_load_dwordx4 v[24:27], v[34:35], off
	global_load_dwordx4 v[28:31], v[34:35], off offset:1024
	v_lshl_add_u64 v[40:41], v[32:33], 0, v[0:1]
	global_load_dwordx4 v[32:35], v[40:41], off
	global_load_dwordx4 v[36:39], v[40:41], off offset:1024
	global_load_dwordx4 v[44:47], v0, s[12:13] offset:1024
	v_lshlrev_b64 v[6:7], 11, v[6:7]
	global_load_dwordx4 v[40:43], v0, s[12:13]
	v_lshl_add_u64 v[6:7], s[18:19], 0, v[6:7]
	global_load_dwordx4 v[48:51], v0, s[14:15]
	v_lshl_add_u64 v[52:53], v[6:7], 0, v[0:1]
	v_mov_b32_e32 v59, 0x3727c5ac
	s_mov_b32 s12, 0xf800000
	v_mov_b32_e32 v60, 0x260
	v_lshl_add_u64 v[4:5], s[4:5], 0, v[4:5]
	v_lshlrev_b64 v[2:3], 10, v[2:3]
	s_waitcnt vmcnt(9)
	v_pk_add_f32 v[54:55], v[12:13], v[8:9]
	v_pk_add_f32 v[56:57], v[14:15], v[10:11]
	s_waitcnt vmcnt(7)
	v_pk_add_f32 v[20:21], v[16:17], v[20:21]
	v_pk_add_f32 v[18:19], v[18:19], v[22:23]
	global_load_dwordx4 v[6:9], v0, s[8:9]
	global_load_dwordx4 v[10:13], v0, s[10:11]
	global_load_dwordx4 v[14:17], v0, s[14:15] offset:1024
	s_waitcnt vmcnt(9)
	v_pk_add_f32 v[54:55], v[54:55], v[24:25]
	v_pk_add_f32 v[26:27], v[56:57], v[26:27]
	s_waitcnt vmcnt(8)
	v_pk_add_f32 v[28:29], v[20:21], v[28:29]
	v_pk_add_f32 v[30:31], v[18:19], v[30:31]
	global_load_dwordx4 v[18:21], v0, s[8:9] offset:1024
	global_load_dwordx4 v[22:25], v0, s[10:11] offset:1024
	s_waitcnt vmcnt(9)
	v_pk_add_f32 v[54:55], v[54:55], v[32:33]
	v_pk_add_f32 v[34:35], v[26:27], v[34:35]
	s_waitcnt vmcnt(8)
	v_pk_add_f32 v[36:37], v[28:29], v[36:37]
	v_pk_add_f32 v[38:39], v[30:31], v[38:39]
	global_load_dwordx4 v[26:29], v[52:53], off
	global_load_dwordx4 v[30:33], v[52:53], off offset:1024
	v_add_f32_e32 v52, 0, v54
	v_add_f32_e32 v52, v52, v55
	v_add_f32_e32 v52, v52, v34
	v_add_f32_e32 v52, v52, v35
	v_add_f32_e32 v52, v52, v36
	v_add_f32_e32 v52, v52, v37
	v_add_f32_e32 v52, v52, v38
	v_add_f32_e32 v52, v52, v39
	s_nop 1
	v_add_f32_dpp v52, v52, v52 quad_perm:[1,0,3,2] row_mask:0xf bank_mask:0xf bound_ctrl:1
	s_nop 1
	v_add_f32_dpp v52, v52, v52 quad_perm:[2,3,0,1] row_mask:0xf bank_mask:0xf bound_ctrl:1
	s_nop 1
	v_add_f32_dpp v52, v52, v52 row_half_mirror row_mask:0xf bank_mask:0xf bound_ctrl:1
	s_nop 1
	v_add_f32_dpp v52, v52, v52 row_mirror row_mask:0xf bank_mask:0xf bound_ctrl:1
	s_nop 0
	v_readlane_b32 s8, v52, 16
	v_readlane_b32 s9, v52, 48
	v_readlane_b32 s0, v52, 0
	v_readlane_b32 s1, v52, 32
	v_mov_b32_e32 v52, s8
	v_mov_b32_e32 v53, s9
	v_pk_add_f32 v[52:53], s[0:1], v[52:53]
	s_nop 0
	v_add_f32_e32 v52, v52, v53
	v_mul_f32_e32 v52, 0x3b000000, v52
	v_pk_add_f32 v[54:55], v[54:55], v[52:53] op_sel_hi:[1,0] neg_lo:[0,1] neg_hi:[0,1]
	v_pk_add_f32 v[34:35], v[34:35], v[52:53] op_sel_hi:[1,0] neg_lo:[0,1] neg_hi:[0,1]
	v_pk_add_f32 v[36:37], v[36:37], v[52:53] op_sel_hi:[1,0] neg_lo:[0,1] neg_hi:[0,1]
	v_pk_add_f32 v[38:39], v[38:39], v[52:53] op_sel_hi:[1,0] neg_lo:[0,1] neg_hi:[0,1]
	v_pk_mul_f32 v[52:53], v[54:55], v[54:55]
	s_waitcnt vmcnt(8)
	v_pk_mul_f32 v[40:41], v[40:41], v[54:55]
	v_add_f32_e32 v56, v52, v53
	v_pk_mul_f32 v[52:53], v[34:35], v[34:35]
	v_pk_mul_f32 v[34:35], v[42:43], v[34:35]
	v_add_f32_e32 v52, v56, v52
	v_add_f32_e32 v56, v52, v53
	v_pk_mul_f32 v[52:53], v[36:37], v[36:37]
	v_pk_mul_f32 v[36:37], v[44:45], v[36:37]
	v_add_f32_e32 v52, v56, v52
	v_add_f32_e32 v56, v52, v53
	v_pk_mul_f32 v[52:53], v[38:39], v[38:39]
	v_pk_mul_f32 v[38:39], v[46:47], v[38:39]
	v_add_f32_e32 v52, v56, v52
	v_add_f32_e32 v52, v52, v53
	s_nop 1
	v_add_f32_dpp v52, v52, v52 quad_perm:[1,0,3,2] row_mask:0xf bank_mask:0xf bound_ctrl:1
	s_nop 1
	v_add_f32_dpp v52, v52, v52 quad_perm:[2,3,0,1] row_mask:0xf bank_mask:0xf bound_ctrl:1
	s_nop 1
	v_add_f32_dpp v52, v52, v52 row_half_mirror row_mask:0xf bank_mask:0xf bound_ctrl:1
	s_nop 1
	v_add_f32_dpp v52, v52, v52 row_mirror row_mask:0xf bank_mask:0xf bound_ctrl:1
	s_nop 0
	v_readlane_b32 s8, v52, 16
	v_readlane_b32 s9, v52, 48
	v_readlane_b32 s0, v52, 0
	v_readlane_b32 s1, v52, 32
	v_mov_b32_e32 v52, s8
	v_mov_b32_e32 v53, s9
	v_pk_add_f32 v[52:53], s[0:1], v[52:53]
	s_nop 0
	v_add_f32_e32 v52, v52, v53
	v_fmamk_f32 v52, v52, 0x3b000000, v59
	v_mul_f32_e32 v53, 0x4f800000, v52
	v_cmp_gt_f32_e32 vcc, s12, v52
	s_nop 1
	v_cndmask_b32_e32 v52, v52, v53, vcc
	v_sqrt_f32_e32 v53, v52
	s_nop 0
	v_add_u32_e32 v42, -1, v53
	v_add_u32_e32 v43, 1, v53
	v_fma_f32 v44, -v42, v53, v52
	v_fma_f32 v45, -v43, v53, v52
	v_cmp_ge_f32_e64 s[0:1], 0, v44
	s_nop 1
	v_cndmask_b32_e64 v42, v53, v42, s[0:1]
	v_cmp_lt_f32_e64 s[0:1], 0, v45
	s_nop 1
	v_cndmask_b32_e64 v42, v42, v43, s[0:1]
	v_mul_f32_e32 v43, 0x37800000, v42
	v_cndmask_b32_e32 v42, v42, v43, vcc
	v_cmp_class_f32_e32 vcc, v52, v60
	s_nop 1
	v_cndmask_b32_e32 v42, v42, v52, vcc
	v_div_scale_f32 v43, s[0:1], v42, v42, 1.0
	v_rcp_f32_e32 v44, v43
	v_div_scale_f32 v45, vcc, 1.0, v42, 1.0
	v_fma_f32 v46, -v43, v44, 1.0
	v_fmac_f32_e32 v44, v46, v44
	v_mul_f32_e32 v46, v45, v44
	v_fma_f32 v47, -v43, v46, v45
	v_fmac_f32_e32 v46, v47, v44
	v_fma_f32 v43, -v43, v46, v45
	v_div_fmas_f32 v43, v43, v44, v46
	v_div_fixup_f32 v42, v43, v42, 1.0
	s_waitcnt vmcnt(7)
	v_pk_fma_f32 v[40:41], v[42:43], v[40:41], v[48:49] op_sel_hi:[0,1,1]
	s_waitcnt vmcnt(4)
	v_pk_fma_f32 v[14:15], v[42:43], v[36:37], v[14:15] op_sel_hi:[0,1,1]
	s_waitcnt vmcnt(1)
	v_pk_add_f32 v[26:27], v[40:41], v[26:27]
	v_pk_fma_f32 v[34:35], v[42:43], v[34:35], v[50:51] op_sel_hi:[0,1,1]
	s_waitcnt vmcnt(0)
	v_pk_add_f32 v[14:15], v[14:15], v[30:31]
	v_add_f32_e32 v30, 0, v26
	v_pk_add_f32 v[28:29], v[34:35], v[28:29]
	v_add_f32_e32 v30, v30, v27
	v_add_f32_e32 v30, v30, v28
	v_add_f32_e32 v30, v30, v29
	v_pk_fma_f32 v[16:17], v[42:43], v[38:39], v[16:17] op_sel_hi:[0,1,1]
	v_add_f32_e32 v30, v30, v14
	v_pk_add_f32 v[16:17], v[16:17], v[32:33]
	v_add_f32_e32 v30, v30, v15
	v_add_f32_e32 v30, v30, v16
	v_add_f32_e32 v30, v30, v17
	s_nop 1
	v_add_f32_dpp v30, v30, v30 quad_perm:[1,0,3,2] row_mask:0xf bank_mask:0xf bound_ctrl:1
	s_nop 1
	v_add_f32_dpp v30, v30, v30 quad_perm:[2,3,0,1] row_mask:0xf bank_mask:0xf bound_ctrl:1
	s_nop 1
	v_add_f32_dpp v30, v30, v30 row_half_mirror row_mask:0xf bank_mask:0xf bound_ctrl:1
	s_nop 1
	v_add_f32_dpp v30, v30, v30 row_mirror row_mask:0xf bank_mask:0xf bound_ctrl:1
	s_nop 0
	v_readlane_b32 s8, v30, 16
	v_readlane_b32 s9, v30, 48
	v_readlane_b32 s0, v30, 0
	v_readlane_b32 s1, v30, 32
	v_mov_b32_e32 v30, s8
	v_mov_b32_e32 v31, s9
	v_pk_add_f32 v[30:31], s[0:1], v[30:31]
	s_nop 0
	v_add_f32_e32 v30, v30, v31
	v_mul_f32_e32 v30, 0x3b000000, v30
	v_pk_add_f32 v[26:27], v[26:27], v[30:31] op_sel_hi:[1,0] neg_lo:[0,1] neg_hi:[0,1]
	v_pk_add_f32 v[28:29], v[28:29], v[30:31] op_sel_hi:[1,0] neg_lo:[0,1] neg_hi:[0,1]
	v_pk_add_f32 v[14:15], v[14:15], v[30:31] op_sel_hi:[1,0] neg_lo:[0,1] neg_hi:[0,1]
	v_pk_add_f32 v[16:17], v[16:17], v[30:31] op_sel_hi:[1,0] neg_lo:[0,1] neg_hi:[0,1]
	v_pk_mul_f32 v[30:31], v[26:27], v[26:27]
	v_pk_mul_f32 v[32:33], v[28:29], v[28:29]
	v_add_f32_e32 v30, v30, v31
	v_add_f32_e32 v30, v30, v32
	v_pk_mul_f32 v[34:35], v[14:15], v[14:15]
	v_add_f32_e32 v30, v30, v33
	v_add_f32_e32 v30, v30, v34
	v_pk_mul_f32 v[36:37], v[16:17], v[16:17]
	v_add_f32_e32 v30, v30, v35
	v_add_f32_e32 v30, v30, v36
	v_add_f32_e32 v30, v30, v37
	s_nop 1
	v_add_f32_dpp v30, v30, v30 quad_perm:[1,0,3,2] row_mask:0xf bank_mask:0xf bound_ctrl:1
	s_nop 1
	v_add_f32_dpp v30, v30, v30 quad_perm:[2,3,0,1] row_mask:0xf bank_mask:0xf bound_ctrl:1
	s_nop 1
	v_add_f32_dpp v30, v30, v30 row_half_mirror row_mask:0xf bank_mask:0xf bound_ctrl:1
	s_nop 1
	v_add_f32_dpp v30, v30, v30 row_mirror row_mask:0xf bank_mask:0xf bound_ctrl:1
	s_nop 0
	v_readlane_b32 s8, v30, 16
	v_readlane_b32 s9, v30, 48
	v_readlane_b32 s0, v30, 0
	v_readlane_b32 s1, v30, 32
	v_mov_b32_e32 v30, s8
	v_mov_b32_e32 v31, s9
	v_pk_add_f32 v[30:31], s[0:1], v[30:31]
	s_nop 0
	v_add_f32_e32 v30, v30, v31
	v_fmac_f32_e32 v59, 0x3b000000, v30
	v_mul_f32_e32 v30, 0x4f800000, v59
	v_cmp_gt_f32_e32 vcc, s12, v59
	s_nop 1
	v_cndmask_b32_e32 v30, v59, v30, vcc
	v_sqrt_f32_e32 v31, v30
	s_nop 0
	v_add_u32_e32 v32, -1, v31
	v_fma_f32 v33, -v32, v31, v30
	v_cmp_ge_f32_e64 s[0:1], 0, v33
	v_add_u32_e32 v33, 1, v31
	s_nop 0
	v_cndmask_b32_e64 v32, v31, v32, s[0:1]
	v_fma_f32 v31, -v33, v31, v30
	v_cmp_lt_f32_e64 s[0:1], 0, v31
	s_nop 1
	v_cndmask_b32_e64 v31, v32, v33, s[0:1]
	v_mul_f32_e32 v32, 0x37800000, v31
	v_cndmask_b32_e32 v31, v31, v32, vcc
	v_cmp_class_f32_e32 vcc, v30, v60
	s_nop 1
	v_cndmask_b32_e32 v32, v31, v30, vcc
	v_div_scale_f32 v33, s[0:1], v32, v32, 1.0
	v_rcp_f32_e32 v34, v33
	v_lshl_add_u64 v[30:31], v[4:5], 0, v[0:1]
	s_mov_b32 s0, 0x43000000
	v_fma_f32 v0, -v33, v34, 1.0
	v_fmac_f32_e32 v34, v0, v34
	v_div_scale_f32 v0, vcc, 1.0, v32, 1.0
	v_mul_f32_e32 v4, v0, v34
	v_fma_f32 v5, -v33, v4, v0
	v_fmac_f32_e32 v4, v5, v34
	v_fma_f32 v0, -v33, v4, v0
	v_div_fmas_f32 v0, v0, v34, v4
	v_div_fixup_f32 v0, v0, v32, 1.0
	v_pk_mul_f32 v[4:5], v[6:7], v[26:27]
	v_pk_mul_f32 v[6:7], v[8:9], v[28:29]
	v_pk_fma_f32 v[4:5], v[0:1], v[4:5], v[10:11] op_sel_hi:[0,1,1]
	v_pk_mul_f32 v[8:9], v[18:19], v[14:15]
	v_pk_fma_f32 v[6:7], v[0:1], v[6:7], v[12:13] op_sel_hi:[0,1,1]
	v_pk_fma_f32 v[8:9], v[0:1], v[8:9], v[22:23] op_sel_hi:[0,1,1]
	v_pk_mul_f32 v[10:11], v[20:21], v[16:17]
	v_fma_mixlo_f16 v12, v4, s0, 0
	v_pk_fma_f32 v[10:11], v[0:1], v[10:11], v[24:25] op_sel_hi:[0,1,1]
	global_store_dwordx4 v[30:31], v[4:7], off sc1
	global_store_dwordx4 v[30:31], v[8:11], off offset:1024 sc1
	v_mul_f32_e32 v0, 0x43000000, v4
	v_fma_mixlo_f16 v4, v4, s0, -v12 op_sel_hi:[0,0,1]
	v_fma_mixlo_f16 v12, v8, s0, 0
	v_mul_f32_e32 v13, 0x43000000, v8
	v_fma_mixlo_f16 v8, v8, s0, -v12 op_sel_hi:[0,0,1]
	v_mul_f32_e32 v12, 0x43000000, v5
	v_fma_mixlo_f16 v14, v5, s0, 0
	v_cvt_pk_f16_f32 v12, v0, v12
	v_mul_f32_e32 v0, 0x43000000, v9
	v_pk_mul_f32 v[16:17], v[6:7], s[0:1] op_sel_hi:[1,0]
	v_fma_mixhi_f16 v4, v5, s0, -v14 op_sel_hi:[0,0,1]
	v_cvt_pk_f16_f32 v14, v13, v0
	v_cvt_pk_f16_f32 v13, v16, v17
	v_pk_mul_f32 v[18:19], v[10:11], s[0:1] op_sel_hi:[1,0]
	v_cvt_f32_f16_e32 v16, v13
	v_cvt_f32_f16_sdwa v17, v13 dst_sel:DWORD dst_unused:UNUSED_PAD src0_sel:WORD_1
	v_cvt_pk_f16_f32 v15, v18, v19
	v_cvt_f32_f16_e32 v18, v15
	v_cvt_f32_f16_sdwa v19, v15 dst_sel:DWORD dst_unused:UNUSED_PAD src0_sel:WORD_1
	v_fma_mixlo_f16 v5, v9, s0, 0
	v_pk_fma_f32 v[6:7], v[6:7], s[0:1], v[16:17] op_sel_hi:[1,0,1] neg_lo:[0,0,1] neg_hi:[0,0,1]
	v_fma_mixhi_f16 v8, v9, s0, -v5 op_sel_hi:[0,0,1]
	v_cvt_pk_f16_f32 v5, v6, v7
	v_pk_fma_f32 v[6:7], v[10:11], s[0:1], v[18:19] op_sel_hi:[1,0,1] neg_lo:[0,0,1] neg_hi:[0,0,1]
	v_lshlrev_b32_e32 v0, 1, v58
	v_cvt_pk_f16_f32 v9, v6, v7
	v_lshl_add_u64 v[6:7], s[6:7], 0, v[2:3]
	v_lshl_add_u64 v[2:3], s[2:3], 0, v[2:3]
	v_lshl_add_u64 v[6:7], v[6:7], 0, v[0:1]
	v_lshl_add_u64 v[0:1], v[2:3], 0, v[0:1]
	v_mbcnt_lo_u32_b32 v20, -1, 0
	v_mbcnt_hi_u32_b32 v20, -1, v20
	v_and_b32_e32 v20, 1, v20
	v_cmp_eq_u32_e32 vcc, 1, v20
	v_mul_u32_u24_e32 v22, 0x1f8, v20
	v_mov_b32_e32 v23, 0
	s_nop 1
	v_mov_b32_dpp v24, v12 quad_perm:[1,0,3,2] row_mask:0xf bank_mask:0xf
	v_mov_b32_dpp v25, v13 quad_perm:[1,0,3,2] row_mask:0xf bank_mask:0xf
	v_mov_b32_dpp v26, v14 quad_perm:[1,0,3,2] row_mask:0xf bank_mask:0xf
	v_mov_b32_dpp v27, v15 quad_perm:[1,0,3,2] row_mask:0xf bank_mask:0xf
	s_nop 1
	v_cndmask_b32_e32 v28, v12, v26, vcc
	v_cndmask_b32_e32 v29, v13, v27, vcc
	v_cndmask_b32_e32 v30, v24, v14, vcc
	v_cndmask_b32_e32 v31, v25, v15, vcc
	v_lshl_add_u64 v[32:33], v[6:7], 0, v[22:23]
	global_store_dwordx4 v[32:33], v[28:31], off sc1
	s_nop 1
	v_mov_b32_dpp v24, v4 quad_perm:[1,0,3,2] row_mask:0xf bank_mask:0xf
	v_mov_b32_dpp v25, v5 quad_perm:[1,0,3,2] row_mask:0xf bank_mask:0xf
	v_mov_b32_dpp v26, v8 quad_perm:[1,0,3,2] row_mask:0xf bank_mask:0xf
	v_mov_b32_dpp v27, v9 quad_perm:[1,0,3,2] row_mask:0xf bank_mask:0xf
	s_nop 1
	v_cndmask_b32_e32 v28, v4, v26, vcc
	v_cndmask_b32_e32 v29, v5, v27, vcc
	v_cndmask_b32_e32 v30, v24, v8, vcc
	v_cndmask_b32_e32 v31, v25, v9, vcc
	v_lshl_add_u64 v[32:33], v[0:1], 0, v[22:23]
	global_store_dwordx4 v[32:33], v[28:31], off sc1
	s_nop 1
	s_endpgm
	s_endpgm
	s_endpgm
	s_endpgm
	s_endpgm
	s_endpgm
	s_endpgm
	s_endpgm
	s_endpgm
	s_endpgm
	s_endpgm
	s_endpgm
	s_endpgm
	s_endpgm
	s_endpgm
	s_endpgm
	s_endpgm
	s_endpgm
	s_endpgm
	s_endpgm
	s_endpgm
	s_endpgm
	s_endpgm
	s_endpgm
	s_endpgm
	s_endpgm
	s_endpgm
	s_endpgm
	s_endpgm
	s_endpgm
	s_endpgm
	s_endpgm
	s_endpgm
	s_endpgm
	s_endpgm
	s_endpgm
	s_endpgm
	s_endpgm
	s_endpgm
	s_endpgm
	s_endpgm
	s_endpgm
	s_endpgm
	s_endpgm
	s_endpgm
	s_endpgm
	s_endpgm
	s_endpgm
	s_endpgm
	s_endpgm
	s_endpgm
	s_endpgm
	s_endpgm

.LBB14_5:
	v_lshlrev_b32_e32 v0, 2, v0
	v_and_b32_e32 v60, 0xfc, v0
	v_lshlrev_b64 v[8:9], 11, v[8:9]
	v_lshlrev_b32_e32 v0, 2, v60
	v_mov_b32_e32 v1, 0
	s_waitcnt lgkmcnt(0)
	v_lshl_add_u64 v[8:9], s[24:25], 0, v[8:9]
	v_lshl_add_u64 v[24:25], v[8:9], 0, v[0:1]
	global_load_dwordx4 v[8:11], v[24:25], off
	global_load_dwordx4 v[12:15], v0, s[20:21]
	global_load_dwordx4 v[16:19], v0, s[20:21] offset:1024
	global_load_dwordx4 v[20:23], v[24:25], off offset:1024
	s_load_dwordx2 s[0:1], s[0:1], 0x8
	v_lshlrev_b64 v[4:5], 11, v[2:3]
	v_lshl_add_u64 v[36:37], s[22:23], 0, v[4:5]
	v_lshl_add_u64 v[28:29], v[36:37], 0, v[0:1]
	global_load_dwordx4 v[24:27], v[28:29], off
	s_waitcnt lgkmcnt(0)
	v_lshl_add_u64 v[30:31], s[0:1], 2, v[36:37]
	v_lshl_add_u64 v[38:39], v[30:31], 0, v[0:1]
	v_lshl_add_u64 v[32:33], s[0:1], 3, v[36:37]
	v_lshl_add_u64 v[44:45], v[32:33], 0, v[0:1]
	global_load_dwordx4 v[32:35], v[38:39], off
	v_mad_u64_u32 v[48:49], s[16:17], s0, 12, v[36:37]
	global_load_dwordx4 v[28:31], v[28:29], off offset:1024
	v_mov_b32_e32 v40, v49
	v_mad_u64_u32 v[46:47], s[0:1], s1, 12, v[40:41]
	global_load_dwordx4 v[40:43], v[44:45], off
	v_mov_b32_e32 v49, v46
	v_lshl_add_u64 v[56:57], v[48:49], 0, v[0:1]
	global_load_dwordx4 v[36:39], v[38:39], off offset:1024
	v_lshlrev_b64 v[6:7], 11, v[6:7]
	global_load_dwordx4 v[44:47], v[44:45], off offset:1024
	s_nop 0
	global_load_dwordx4 v[48:51], v[56:57], off
	global_load_dwordx4 v[52:55], v[56:57], off offset:1024
	v_lshl_add_u64 v[6:7], s[18:19], 0, v[6:7]
	v_lshl_add_u64 v[56:57], v[6:7], 0, v[0:1]
	v_mov_b32_e32 v61, 0x3727c5ac
	s_mov_b32 s16, 0xf800000
	v_lshl_add_u64 v[4:5], s[4:5], 0, v[4:5]
	v_lshlrev_b64 v[2:3], 10, v[2:3]
	s_waitcnt vmcnt(10)
	v_pk_add_f32 v[58:59], v[12:13], v[8:9]
	v_pk_add_f32 v[14:15], v[14:15], v[10:11]
	global_load_dwordx4 v[6:9], v0, s[12:13]
	global_load_dwordx4 v[10:13], v0, s[14:15]
	s_waitcnt vmcnt(10)
	v_pk_add_f32 v[16:17], v[16:17], v[20:21]
	v_pk_add_f32 v[18:19], v[18:19], v[22:23]
	s_waitcnt vmcnt(9)
	v_pk_add_f32 v[22:23], v[58:59], v[24:25]
	v_pk_add_f32 v[24:25], v[14:15], v[26:27]
	s_waitcnt vmcnt(8)
	v_pk_add_f32 v[32:33], v[22:23], v[32:33]
	v_pk_add_f32 v[34:35], v[24:25], v[34:35]
	s_waitcnt vmcnt(7)
	v_pk_add_f32 v[58:59], v[16:17], v[28:29]
	v_pk_add_f32 v[30:31], v[18:19], v[30:31]
	global_load_dwordx4 v[14:17], v0, s[12:13] offset:1024
	global_load_dwordx4 v[18:21], v0, s[14:15] offset:1024
	global_load_dwordx4 v[22:25], v[56:57], off
	global_load_dwordx4 v[26:29], v[56:57], off offset:1024
	s_waitcnt vmcnt(10)
	v_pk_add_f32 v[32:33], v[32:33], v[40:41]
	v_pk_add_f32 v[34:35], v[34:35], v[42:43]
	s_waitcnt vmcnt(9)
	v_pk_add_f32 v[30:31], v[30:31], v[38:39]
	v_pk_add_f32 v[36:37], v[58:59], v[36:37]
	s_waitcnt vmcnt(7)
	v_pk_add_f32 v[32:33], v[32:33], v[48:49]
	v_pk_add_f32 v[34:35], v[34:35], v[50:51]
	v_add_f32_e32 v38, 0, v32
	v_add_f32_e32 v38, v38, v33
	v_pk_add_f32 v[36:37], v[36:37], v[44:45]
	v_add_f32_e32 v38, v38, v34
	s_waitcnt vmcnt(6)
	v_pk_add_f32 v[36:37], v[36:37], v[52:53]
	v_add_f32_e32 v38, v38, v35
	v_pk_add_f32 v[30:31], v[30:31], v[46:47]
	v_add_f32_e32 v38, v38, v36
	v_pk_add_f32 v[30:31], v[30:31], v[54:55]
	v_add_f32_e32 v38, v38, v37
	v_add_f32_e32 v38, v38, v30
	v_add_f32_e32 v38, v38, v31
	v_mov_b32_e32 v55, 0x260
	s_nop 0
	v_add_f32_dpp v38, v38, v38 quad_perm:[1,0,3,2] row_mask:0xf bank_mask:0xf bound_ctrl:1
	s_nop 1
	v_add_f32_dpp v38, v38, v38 quad_perm:[2,3,0,1] row_mask:0xf bank_mask:0xf bound_ctrl:1
	s_nop 1
	v_add_f32_dpp v38, v38, v38 row_half_mirror row_mask:0xf bank_mask:0xf bound_ctrl:1
	s_nop 1
	v_add_f32_dpp v38, v38, v38 row_mirror row_mask:0xf bank_mask:0xf bound_ctrl:1
	s_nop 0
	v_readlane_b32 s12, v38, 16
	v_readlane_b32 s13, v38, 48
	v_readlane_b32 s0, v38, 0
	v_readlane_b32 s1, v38, 32
	v_mov_b32_e32 v38, s12
	v_mov_b32_e32 v39, s13
	v_pk_add_f32 v[38:39], s[0:1], v[38:39]
	s_nop 0
	v_add_f32_e32 v38, v38, v39
	v_mul_f32_e32 v38, 0x3b000000, v38
	v_pk_add_f32 v[46:47], v[32:33], v[38:39] op_sel_hi:[1,0] neg_lo:[0,1] neg_hi:[0,1]
	v_pk_add_f32 v[48:49], v[34:35], v[38:39] op_sel_hi:[1,0] neg_lo:[0,1] neg_hi:[0,1]
	v_pk_add_f32 v[52:53], v[30:31], v[38:39] op_sel_hi:[1,0] neg_lo:[0,1] neg_hi:[0,1]
	v_pk_mul_f32 v[30:31], v[46:47], v[46:47]
	v_pk_mul_f32 v[32:33], v[48:49], v[48:49]
	v_add_f32_e32 v30, v30, v31
	v_pk_add_f32 v[50:51], v[36:37], v[38:39] op_sel_hi:[1,0] neg_lo:[0,1] neg_hi:[0,1]
	v_add_f32_e32 v30, v30, v32
	v_pk_mul_f32 v[34:35], v[50:51], v[50:51]
	v_add_f32_e32 v30, v30, v33
	v_add_f32_e32 v30, v30, v34
	v_pk_mul_f32 v[36:37], v[52:53], v[52:53]
	v_add_f32_e32 v30, v30, v35
	v_add_f32_e32 v30, v30, v36
	v_add_f32_e32 v30, v30, v37
	s_waitcnt vmcnt(5)
	v_pk_mul_f32 v[6:7], v[6:7], v[46:47]
	v_add_f32_dpp v30, v30, v30 quad_perm:[1,0,3,2] row_mask:0xf bank_mask:0xf bound_ctrl:1
	v_pk_mul_f32 v[8:9], v[8:9], v[48:49]
	s_nop 0
	v_add_f32_dpp v30, v30, v30 quad_perm:[2,3,0,1] row_mask:0xf bank_mask:0xf bound_ctrl:1
	s_nop 1
	v_add_f32_dpp v30, v30, v30 row_half_mirror row_mask:0xf bank_mask:0xf bound_ctrl:1
	s_nop 1
	v_add_f32_dpp v30, v30, v30 row_mirror row_mask:0xf bank_mask:0xf bound_ctrl:1
	s_nop 0
	v_readlane_b32 s12, v30, 16
	v_readlane_b32 s13, v30, 48
	v_readlane_b32 s0, v30, 0
	v_readlane_b32 s1, v30, 32
	v_mov_b32_e32 v30, s12
	v_mov_b32_e32 v31, s13
	v_pk_add_f32 v[30:31], s[0:1], v[30:31]
	s_nop 0
	v_add_f32_e32 v30, v30, v31
	v_fmamk_f32 v30, v30, 0x3b000000, v61
	v_mul_f32_e32 v31, 0x4f800000, v30
	v_cmp_gt_f32_e32 vcc, s16, v30
	s_nop 1
	v_cndmask_b32_e32 v54, v30, v31, vcc
	v_sqrt_f32_e32 v38, v54
	global_load_dwordx4 v[30:33], v0, s[8:9]
	global_load_dwordx4 v[34:37], v0, s[10:11]
	v_add_u32_e32 v39, -1, v38
	v_add_u32_e32 v56, 1, v38
	v_fma_f32 v40, -v39, v38, v54
	v_fma_f32 v41, -v56, v38, v54
	v_cmp_ge_f32_e64 s[0:1], 0, v40
	s_nop 1
	v_cndmask_b32_e64 v57, v38, v39, s[0:1]
	v_cmp_lt_f32_e64 s[0:1], 0, v41
	global_load_dwordx4 v[38:41], v0, s[8:9] offset:1024
	global_load_dwordx4 v[42:45], v0, s[10:11] offset:1024
	v_cndmask_b32_e64 v46, v57, v56, s[0:1]
	v_mul_f32_e32 v47, 0x37800000, v46
	v_cndmask_b32_e32 v46, v46, v47, vcc
	v_cmp_class_f32_e32 vcc, v54, v55
	s_nop 1
	v_cndmask_b32_e32 v46, v46, v54, vcc
	v_div_scale_f32 v47, s[0:1], v46, v46, 1.0
	v_rcp_f32_e32 v54, v47
	v_div_scale_f32 v48, vcc, 1.0, v46, 1.0
	v_fma_f32 v49, -v47, v54, 1.0
	v_fmac_f32_e32 v54, v49, v54
	v_mul_f32_e32 v49, v48, v54
	v_fma_f32 v56, -v47, v49, v48
	v_fmac_f32_e32 v49, v56, v54
	v_fma_f32 v47, -v47, v49, v48
	v_div_fmas_f32 v47, v47, v54, v49
	v_div_fixup_f32 v46, v47, v46, 1.0
	s_waitcnt vmcnt(8)
	v_pk_fma_f32 v[6:7], v[46:47], v[6:7], v[10:11] op_sel_hi:[0,1,1]
	s_waitcnt vmcnt(5)
	v_pk_add_f32 v[6:7], v[6:7], v[22:23]
	v_pk_fma_f32 v[8:9], v[46:47], v[8:9], v[12:13] op_sel_hi:[0,1,1]
	v_pk_mul_f32 v[10:11], v[14:15], v[50:51]
	v_add_f32_e32 v14, 0, v6
	v_add_f32_e32 v14, v14, v7
	v_pk_add_f32 v[8:9], v[8:9], v[24:25]
	v_pk_fma_f32 v[10:11], v[46:47], v[10:11], v[18:19] op_sel_hi:[0,1,1]
	v_add_f32_e32 v14, v14, v8
	v_pk_mul_f32 v[12:13], v[16:17], v[52:53]
	v_add_f32_e32 v14, v14, v9
	s_waitcnt vmcnt(4)
	v_pk_add_f32 v[10:11], v[10:11], v[26:27]
	v_pk_fma_f32 v[12:13], v[46:47], v[12:13], v[20:21] op_sel_hi:[0,1,1]
	v_add_f32_e32 v14, v14, v10
	v_add_f32_e32 v14, v14, v11
	v_pk_add_f32 v[12:13], v[12:13], v[28:29]
	s_nop 0
	v_add_f32_e32 v14, v14, v12
	v_add_f32_e32 v14, v14, v13
	s_nop 1
	v_add_f32_dpp v14, v14, v14 quad_perm:[1,0,3,2] row_mask:0xf bank_mask:0xf bound_ctrl:1
	s_nop 1
	v_add_f32_dpp v14, v14, v14 quad_perm:[2,3,0,1] row_mask:0xf bank_mask:0xf bound_ctrl:1
	s_nop 1
	v_add_f32_dpp v14, v14, v14 row_half_mirror row_mask:0xf bank_mask:0xf bound_ctrl:1
	s_nop 1
	v_add_f32_dpp v14, v14, v14 row_mirror row_mask:0xf bank_mask:0xf bound_ctrl:1
	s_nop 0
	v_readlane_b32 s8, v14, 16
	v_readlane_b32 s9, v14, 48
	v_readlane_b32 s0, v14, 0
	v_readlane_b32 s1, v14, 32
	v_mov_b32_e32 v14, s8
	v_mov_b32_e32 v15, s9
	v_pk_add_f32 v[14:15], s[0:1], v[14:15]
	s_nop 0
	v_add_f32_e32 v14, v14, v15
	v_mul_f32_e32 v14, 0x3b000000, v14
	v_pk_add_f32 v[6:7], v[6:7], v[14:15] op_sel_hi:[1,0] neg_lo:[0,1] neg_hi:[0,1]
	v_pk_add_f32 v[8:9], v[8:9], v[14:15] op_sel_hi:[1,0] neg_lo:[0,1] neg_hi:[0,1]
	v_pk_mul_f32 v[16:17], v[6:7], v[6:7]
	v_pk_mul_f32 v[18:19], v[8:9], v[8:9]
	v_add_f32_e32 v16, v16, v17
	v_pk_add_f32 v[10:11], v[10:11], v[14:15] op_sel_hi:[1,0] neg_lo:[0,1] neg_hi:[0,1]
	v_add_f32_e32 v16, v16, v18
	v_pk_mul_f32 v[20:21], v[10:11], v[10:11]
	v_add_f32_e32 v16, v16, v19
	v_pk_add_f32 v[12:13], v[12:13], v[14:15] op_sel_hi:[1,0] neg_lo:[0,1] neg_hi:[0,1]
	v_add_f32_e32 v16, v16, v20
	v_pk_mul_f32 v[14:15], v[12:13], v[12:13]
	v_add_f32_e32 v16, v16, v21
	v_add_f32_e32 v14, v16, v14
	v_add_f32_e32 v14, v14, v15
	s_nop 1
	v_add_f32_dpp v14, v14, v14 quad_perm:[1,0,3,2] row_mask:0xf bank_mask:0xf bound_ctrl:1
	s_nop 1
	v_add_f32_dpp v14, v14, v14 quad_perm:[2,3,0,1] row_mask:0xf bank_mask:0xf bound_ctrl:1
	s_nop 1
	v_add_f32_dpp v14, v14, v14 row_half_mirror row_mask:0xf bank_mask:0xf bound_ctrl:1
	s_nop 1
	v_add_f32_dpp v14, v14, v14 row_mirror row_mask:0xf bank_mask:0xf bound_ctrl:1
	s_nop 0
	v_readlane_b32 s8, v14, 16
	v_readlane_b32 s9, v14, 48
	v_readlane_b32 s0, v14, 0
	v_readlane_b32 s1, v14, 32
	v_mov_b32_e32 v14, s8
	v_mov_b32_e32 v15, s9
	v_pk_add_f32 v[14:15], s[0:1], v[14:15]
	s_nop 0
	v_add_f32_e32 v14, v14, v15
	v_fmac_f32_e32 v61, 0x3b000000, v14
	v_mul_f32_e32 v14, 0x4f800000, v61
	v_cmp_gt_f32_e32 vcc, s16, v61
	s_nop 1
	v_cndmask_b32_e32 v14, v61, v14, vcc
	v_sqrt_f32_e32 v15, v14
	s_nop 0
	v_add_u32_e32 v16, -1, v15
	v_fma_f32 v17, -v16, v15, v14
	v_cmp_ge_f32_e64 s[0:1], 0, v17
	v_add_u32_e32 v17, 1, v15
	s_nop 0
	v_cndmask_b32_e64 v16, v15, v16, s[0:1]
	v_fma_f32 v15, -v17, v15, v14
	v_cmp_lt_f32_e64 s[0:1], 0, v15
	s_nop 1
	v_cndmask_b32_e64 v15, v16, v17, s[0:1]
	v_mul_f32_e32 v16, 0x37800000, v15
	v_cndmask_b32_e32 v15, v15, v16, vcc
	v_cmp_class_f32_e32 vcc, v14, v55
	s_nop 1
	v_cndmask_b32_e32 v16, v15, v14, vcc
	v_div_scale_f32 v17, s[0:1], v16, v16, 1.0
	v_rcp_f32_e32 v18, v17
	v_lshl_add_u64 v[14:15], v[4:5], 0, v[0:1]
	s_mov_b32 s0, 0x43000000
	v_fma_f32 v0, -v17, v18, 1.0
	v_fmac_f32_e32 v18, v0, v18
	v_div_scale_f32 v0, vcc, 1.0, v16, 1.0
	v_mul_f32_e32 v4, v0, v18
	v_fma_f32 v5, -v17, v4, v0
	v_fmac_f32_e32 v4, v5, v18
	v_fma_f32 v0, -v17, v4, v0
	v_div_fmas_f32 v0, v0, v18, v4
	v_div_fixup_f32 v0, v0, v16, 1.0
	s_waitcnt vmcnt(3)
	v_pk_mul_f32 v[4:5], v[30:31], v[6:7]
	v_pk_mul_f32 v[6:7], v[32:33], v[8:9]
	s_waitcnt vmcnt(2)
	v_pk_fma_f32 v[4:5], v[0:1], v[4:5], v[34:35] op_sel_hi:[0,1,1]
	s_waitcnt vmcnt(1)
	v_pk_mul_f32 v[8:9], v[38:39], v[10:11]
	v_pk_fma_f32 v[6:7], v[0:1], v[6:7], v[36:37] op_sel_hi:[0,1,1]
	s_waitcnt vmcnt(0)
	v_pk_fma_f32 v[8:9], v[0:1], v[8:9], v[42:43] op_sel_hi:[0,1,1]
	v_pk_mul_f32 v[10:11], v[40:41], v[12:13]
	v_fma_mixlo_f16 v12, v4, s0, 0
	v_pk_fma_f32 v[10:11], v[0:1], v[10:11], v[44:45] op_sel_hi:[0,1,1]
	global_store_dwordx4 v[14:15], v[4:7], off sc1
	global_store_dwordx4 v[14:15], v[8:11], off offset:1024 sc1
	v_mul_f32_e32 v0, 0x43000000, v4
	v_fma_mixlo_f16 v4, v4, s0, -v12 op_sel_hi:[0,0,1]
	v_fma_mixlo_f16 v12, v8, s0, 0
	v_mul_f32_e32 v13, 0x43000000, v8
	v_fma_mixlo_f16 v8, v8, s0, -v12 op_sel_hi:[0,0,1]
	v_mul_f32_e32 v12, 0x43000000, v5
	v_fma_mixlo_f16 v14, v5, s0, 0
	v_cvt_pk_f16_f32 v12, v0, v12
	v_mul_f32_e32 v0, 0x43000000, v9
	v_pk_mul_f32 v[16:17], v[6:7], s[0:1] op_sel_hi:[1,0]
	v_fma_mixhi_f16 v4, v5, s0, -v14 op_sel_hi:[0,0,1]
	v_cvt_pk_f16_f32 v14, v13, v0
	v_cvt_pk_f16_f32 v13, v16, v17
	v_pk_mul_f32 v[18:19], v[10:11], s[0:1] op_sel_hi:[1,0]
	v_cvt_f32_f16_e32 v16, v13
	v_cvt_f32_f16_sdwa v17, v13 dst_sel:DWORD dst_unused:UNUSED_PAD src0_sel:WORD_1
	v_cvt_pk_f16_f32 v15, v18, v19
	v_cvt_f32_f16_e32 v18, v15
	v_cvt_f32_f16_sdwa v19, v15 dst_sel:DWORD dst_unused:UNUSED_PAD src0_sel:WORD_1
	v_fma_mixlo_f16 v5, v9, s0, 0
	v_pk_fma_f32 v[6:7], v[6:7], s[0:1], v[16:17] op_sel_hi:[1,0,1] neg_lo:[0,0,1] neg_hi:[0,0,1]
	v_fma_mixhi_f16 v8, v9, s0, -v5 op_sel_hi:[0,0,1]
	v_cvt_pk_f16_f32 v5, v6, v7
	v_pk_fma_f32 v[6:7], v[10:11], s[0:1], v[18:19] op_sel_hi:[1,0,1] neg_lo:[0,0,1] neg_hi:[0,0,1]
	v_lshlrev_b32_e32 v0, 1, v60
	v_cvt_pk_f16_f32 v9, v6, v7
	v_lshl_add_u64 v[6:7], s[6:7], 0, v[2:3]
	v_lshl_add_u64 v[2:3], s[2:3], 0, v[2:3]
	v_lshl_add_u64 v[6:7], v[6:7], 0, v[0:1]
	v_lshl_add_u64 v[0:1], v[2:3], 0, v[0:1]
	v_mbcnt_lo_u32_b32 v20, -1, 0
	v_mbcnt_hi_u32_b32 v20, -1, v20
	v_and_b32_e32 v20, 1, v20
	v_cmp_eq_u32_e32 vcc, 1, v20
	v_mul_u32_u24_e32 v22, 0x1f8, v20
	v_mov_b32_e32 v23, 0
	s_nop 1
	v_mov_b32_dpp v24, v12 quad_perm:[1,0,3,2] row_mask:0xf bank_mask:0xf
	v_mov_b32_dpp v25, v13 quad_perm:[1,0,3,2] row_mask:0xf bank_mask:0xf
	v_mov_b32_dpp v26, v14 quad_perm:[1,0,3,2] row_mask:0xf bank_mask:0xf
	v_mov_b32_dpp v27, v15 quad_perm:[1,0,3,2] row_mask:0xf bank_mask:0xf
	s_nop 1
	v_cndmask_b32_e32 v28, v12, v26, vcc
	v_cndmask_b32_e32 v29, v13, v27, vcc
	v_cndmask_b32_e32 v30, v24, v14, vcc
	v_cndmask_b32_e32 v31, v25, v15, vcc
	v_lshl_add_u64 v[32:33], v[6:7], 0, v[22:23]
	global_store_dwordx4 v[32:33], v[28:31], off sc1
	s_nop 1
	v_mov_b32_dpp v24, v4 quad_perm:[1,0,3,2] row_mask:0xf bank_mask:0xf
	v_mov_b32_dpp v25, v5 quad_perm:[1,0,3,2] row_mask:0xf bank_mask:0xf
	v_mov_b32_dpp v26, v8 quad_perm:[1,0,3,2] row_mask:0xf bank_mask:0xf
	v_mov_b32_dpp v27, v9 quad_perm:[1,0,3,2] row_mask:0xf bank_mask:0xf
	s_nop 1
	v_cndmask_b32_e32 v28, v4, v26, vcc
	v_cndmask_b32_e32 v29, v5, v27, vcc
	v_cndmask_b32_e32 v30, v24, v8, vcc
	v_cndmask_b32_e32 v31, v25, v9, vcc
	v_lshl_add_u64 v[32:33], v[0:1], 0, v[22:23]
	global_store_dwordx4 v[32:33], v[28:31], off sc1
	s_nop 1
	s_endpgm
	s_endpgm
	s_endpgm
	s_endpgm
	s_endpgm
	s_endpgm
	s_endpgm
	s_endpgm
	s_endpgm
	s_endpgm
	s_endpgm

.LBB15_5:
	v_lshlrev_b32_e32 v0, 2, v0
	v_and_b32_e32 v8, 0xfc, v0
	v_lshlrev_b64 v[4:5], 11, v[4:5]
	v_lshlrev_b32_e32 v0, 2, v8
	v_mov_b32_e32 v1, 0
	s_waitcnt lgkmcnt(0)
	v_lshl_add_u64 v[4:5], s[24:25], 0, v[4:5]
	v_lshl_add_u64 v[4:5], v[4:5], 0, v[0:1]
	global_load_dwordx4 v[10:13], v[4:5], off
	global_load_dwordx4 v[14:17], v0, s[20:21]
	global_load_dwordx4 v[18:21], v0, s[20:21] offset:1024
	global_load_dwordx4 v[22:25], v[4:5], off offset:1024
	s_load_dwordx2 s[0:1], s[0:1], 0x8
	v_lshlrev_b64 v[4:5], 11, v[2:3]
	v_lshl_add_u64 v[50:51], s[22:23], 0, v[4:5]
	v_lshl_add_u64 v[30:31], v[50:51], 0, v[0:1]
	global_load_dwordx4 v[26:29], v[30:31], off
	s_waitcnt lgkmcnt(0)
	v_lshl_add_u64 v[34:35], s[0:1], 2, v[50:51]
	global_load_dwordx4 v[30:33], v[30:31], off offset:1024
	v_lshl_add_u64 v[42:43], v[34:35], 0, v[0:1]
	global_load_dwordx4 v[34:37], v[42:43], off
	global_load_dwordx4 v[38:41], v[42:43], off offset:1024
	v_lshl_add_u64 v[42:43], s[0:1], 3, v[50:51]
	v_lshl_add_u64 v[52:53], v[42:43], 0, v[0:1]
	global_load_dwordx4 v[42:45], v[52:53], off
	global_load_dwordx4 v[46:49], v[52:53], off offset:1024
	v_mad_u64_u32 v[52:53], s[16:17], s0, 12, v[50:51]
	v_mad_u64_u32 v[56:57], s[16:17], s0, 20, v[50:51]
	v_mad_u64_u32 v[62:63], s[16:17], s0, 24, v[50:51]
	v_lshl_add_u64 v[54:55], s[0:1], 4, v[50:51]
	v_mad_u64_u32 v[50:51], s[16:17], s0, 28, v[50:51]
	v_lshl_add_u64 v[54:55], v[54:55], 0, v[0:1]
	v_lshlrev_b64 v[6:7], 11, v[6:7]
	v_lshl_add_u64 v[6:7], s[18:19], 0, v[6:7]
	v_lshl_add_u64 v[6:7], v[6:7], 0, v[0:1]
	v_lshl_add_u64 v[4:5], s[4:5], 0, v[4:5]
	v_lshlrev_b64 v[2:3], 10, v[2:3]
	s_waitcnt vmcnt(8)
	v_pk_add_f32 v[58:59], v[14:15], v[10:11]
	v_mov_b32_e32 v10, v53
	v_pk_add_f32 v[60:61], v[16:17], v[12:13]
	v_mov_b32_e32 v12, v57
	v_mad_u64_u32 v[10:11], s[16:17], s1, 12, v[10:11]
	v_mov_b32_e32 v53, v10
	v_mov_b32_e32 v10, v63
	v_mad_u64_u32 v[12:13], s[16:17], s1, 20, v[12:13]
	v_mov_b32_e32 v57, v12
	v_mov_b32_e32 v12, v51
	v_mad_u64_u32 v[10:11], s[16:17], s1, 24, v[10:11]
	s_waitcnt vmcnt(6)
	v_pk_add_f32 v[66:67], v[18:19], v[22:23]
	v_lshl_add_u64 v[22:23], v[52:53], 0, v[0:1]
	v_mad_u64_u32 v[64:65], s[0:1], s1, 28, v[12:13]
	v_mov_b32_e32 v63, v10
	v_pk_add_f32 v[68:69], v[20:21], v[24:25]
	global_load_dwordx4 v[10:13], v[54:55], off
	global_load_dwordx4 v[14:17], v[54:55], off offset:1024
	global_load_dwordx4 v[18:21], v[22:23], off
	v_lshl_add_u64 v[52:53], v[56:57], 0, v[0:1]
	s_waitcnt vmcnt(8)
	v_pk_add_f32 v[54:55], v[58:59], v[26:27]
	v_pk_add_f32 v[56:57], v[60:61], v[28:29]
	global_load_dwordx4 v[26:29], v[52:53], off
	v_lshl_add_u64 v[58:59], v[62:63], 0, v[0:1]
	global_load_dwordx4 v[22:25], v[22:23], off offset:1024
	v_mov_b32_e32 v51, v64
	s_waitcnt vmcnt(9)
	v_pk_add_f32 v[60:61], v[66:67], v[30:31]
	v_pk_add_f32 v[62:63], v[68:69], v[32:33]
	s_waitcnt vmcnt(8)
	v_pk_add_f32 v[54:55], v[54:55], v[34:35]
	v_pk_add_f32 v[56:57], v[56:57], v[36:37]
	global_load_dwordx4 v[30:33], v[52:53], off offset:1024
	global_load_dwordx4 v[34:37], v[58:59], off
	v_lshl_add_u64 v[50:51], v[50:51], 0, v[0:1]
	s_waitcnt vmcnt(9)
	v_pk_add_f32 v[52:53], v[60:61], v[38:39]
	v_pk_add_f32 v[60:61], v[62:63], v[40:41]
	s_waitcnt vmcnt(8)
	v_pk_add_f32 v[54:55], v[54:55], v[42:43]
	v_pk_add_f32 v[56:57], v[56:57], v[44:45]
	global_load_dwordx4 v[38:41], v[50:51], off
	global_load_dwordx4 v[42:45], v[58:59], off offset:1024
	s_waitcnt vmcnt(9)
	v_pk_add_f32 v[52:53], v[52:53], v[46:47]
	v_pk_add_f32 v[58:59], v[60:61], v[48:49]
	global_load_dwordx4 v[46:49], v[50:51], off offset:1024
	s_waitcnt vmcnt(7)
	v_pk_add_f32 v[18:19], v[54:55], v[18:19]
	s_nop 0
	v_pk_add_f32 v[10:11], v[18:19], v[10:11]
	v_pk_add_f32 v[20:21], v[56:57], v[20:21]
	v_mov_b32_e32 v57, 0x3727c5ac
	s_waitcnt vmcnt(6)
	v_pk_add_f32 v[18:19], v[10:11], v[26:27]
	v_pk_add_f32 v[12:13], v[20:21], v[12:13]
	s_waitcnt vmcnt(5)
	v_pk_add_f32 v[22:23], v[52:53], v[22:23]
	v_pk_add_f32 v[10:11], v[58:59], v[24:25]
	v_pk_add_f32 v[14:15], v[22:23], v[14:15]
	v_pk_add_f32 v[10:11], v[10:11], v[16:17]
	v_pk_add_f32 v[20:21], v[12:13], v[28:29]
	v_mov_b32_e32 v58, 0x260
	s_waitcnt vmcnt(4)
	v_pk_add_f32 v[50:51], v[14:15], v[30:31]
	v_pk_add_f32 v[52:53], v[10:11], v[32:33]
	global_load_dwordx4 v[10:13], v0, s[12:13]
	global_load_dwordx4 v[14:17], v0, s[14:15]
	s_waitcnt vmcnt(5)
	v_pk_add_f32 v[18:19], v[18:19], v[34:35]
	s_waitcnt vmcnt(4)
	v_pk_add_f32 v[34:35], v[18:19], v[38:39]
	v_pk_add_f32 v[18:19], v[20:21], v[36:37]
	v_add_f32_e32 v9, 0, v34
	v_pk_add_f32 v[36:37], v[18:19], v[40:41]
	global_load_dwordx4 v[18:21], v0, s[12:13] offset:1024
	global_load_dwordx4 v[22:25], v0, s[14:15] offset:1024
	global_load_dwordx4 v[26:29], v[6:7], off
	global_load_dwordx4 v[30:33], v[6:7], off offset:1024
	v_add_f32_e32 v9, v9, v35
	v_add_f32_e32 v9, v9, v36
	s_waitcnt vmcnt(7)
	v_pk_add_f32 v[6:7], v[50:51], v[42:43]
	v_add_f32_e32 v9, v9, v37
	s_waitcnt vmcnt(6)
	v_pk_add_f32 v[6:7], v[6:7], v[46:47]
	v_pk_add_f32 v[38:39], v[52:53], v[44:45]
	v_add_f32_e32 v9, v9, v6
	v_add_f32_e32 v9, v9, v7
	v_pk_add_f32 v[38:39], v[38:39], v[48:49]
	s_nop 0
	v_add_f32_e32 v9, v9, v38
	v_add_f32_e32 v9, v9, v39
	s_nop 1
	v_add_f32_dpp v9, v9, v9 quad_perm:[1,0,3,2] row_mask:0xf bank_mask:0xf bound_ctrl:1
	s_nop 1
	v_add_f32_dpp v9, v9, v9 quad_perm:[2,3,0,1] row_mask:0xf bank_mask:0xf bound_ctrl:1
	s_nop 1
	v_add_f32_dpp v9, v9, v9 row_half_mirror row_mask:0xf bank_mask:0xf bound_ctrl:1
	s_nop 1
	v_add_f32_dpp v9, v9, v9 row_mirror row_mask:0xf bank_mask:0xf bound_ctrl:1
	s_nop 0
	v_readlane_b32 s12, v9, 16
	v_readlane_b32 s13, v9, 48
	v_readlane_b32 s0, v9, 0
	v_readlane_b32 s1, v9, 32
	v_mov_b32_e32 v40, s12
	v_mov_b32_e32 v41, s13
	v_pk_add_f32 v[40:41], s[0:1], v[40:41]
	s_nop 0
	v_add_f32_e32 v9, v40, v41
	v_mul_f32_e32 v40, 0x3b000000, v9
	v_pk_add_f32 v[50:51], v[34:35], v[40:41] op_sel_hi:[1,0] neg_lo:[0,1] neg_hi:[0,1]
	v_pk_add_f32 v[52:53], v[36:37], v[40:41] op_sel_hi:[1,0] neg_lo:[0,1] neg_hi:[0,1]
	v_pk_mul_f32 v[34:35], v[50:51], v[50:51]
	v_pk_mul_f32 v[36:37], v[52:53], v[52:53]
	v_add_f32_e32 v9, v34, v35
	v_pk_add_f32 v[6:7], v[6:7], v[40:41] op_sel_hi:[1,0] neg_lo:[0,1] neg_hi:[0,1]
	v_add_f32_e32 v9, v9, v36
	v_pk_mul_f32 v[42:43], v[6:7], v[6:7]
	v_add_f32_e32 v9, v9, v37
	v_pk_add_f32 v[54:55], v[38:39], v[40:41] op_sel_hi:[1,0] neg_lo:[0,1] neg_hi:[0,1]
	v_add_f32_e32 v9, v9, v42
	v_pk_mul_f32 v[38:39], v[54:55], v[54:55]
	v_add_f32_e32 v9, v9, v43
	v_add_f32_e32 v9, v9, v38
	v_add_f32_e32 v9, v9, v39
	s_waitcnt vmcnt(5)
	v_pk_mul_f32 v[10:11], v[10:11], v[50:51]
	v_add_f32_dpp v9, v9, v9 quad_perm:[1,0,3,2] row_mask:0xf bank_mask:0xf bound_ctrl:1
	v_pk_mul_f32 v[12:13], v[12:13], v[52:53]
	s_waitcnt vmcnt(3)
	v_pk_mul_f32 v[6:7], v[18:19], v[6:7]
	v_add_f32_dpp v9, v9, v9 quad_perm:[2,3,0,1] row_mask:0xf bank_mask:0xf bound_ctrl:1
	s_nop 1
	v_add_f32_dpp v9, v9, v9 row_half_mirror row_mask:0xf bank_mask:0xf bound_ctrl:1
	s_nop 1
	v_add_f32_dpp v9, v9, v9 row_mirror row_mask:0xf bank_mask:0xf bound_ctrl:1
	s_nop 0
	v_readlane_b32 s12, v9, 16
	v_readlane_b32 s13, v9, 48
	v_readlane_b32 s0, v9, 0
	v_readlane_b32 s1, v9, 32
	v_mov_b32_e32 v34, s12
	v_mov_b32_e32 v35, s13
	v_pk_add_f32 v[34:35], s[0:1], v[34:35]
	s_mov_b32 s12, 0xf800000
	v_add_f32_e32 v9, v34, v35
	v_fmamk_f32 v9, v9, 0x3b000000, v57
	v_mul_f32_e32 v34, 0x4f800000, v9
	v_cmp_gt_f32_e32 vcc, s12, v9
	s_nop 1
	v_cndmask_b32_e32 v9, v9, v34, vcc
	v_sqrt_f32_e32 v34, v9
	s_nop 0
	v_add_u32_e32 v35, -1, v34
	v_fma_f32 v36, -v35, v34, v9
	v_cmp_ge_f32_e64 s[0:1], 0, v36
	v_add_u32_e32 v36, 1, v34
	s_nop 0
	v_cndmask_b32_e64 v35, v34, v35, s[0:1]
	v_fma_f32 v34, -v36, v34, v9
	v_cmp_lt_f32_e64 s[0:1], 0, v34
	s_nop 1
	v_cndmask_b32_e64 v34, v35, v36, s[0:1]
	v_mul_f32_e32 v35, 0x37800000, v34
	v_cndmask_b32_e32 v34, v34, v35, vcc
	v_cmp_class_f32_e32 vcc, v9, v58
	s_nop 1
	v_cndmask_b32_e32 v9, v34, v9, vcc
	v_div_scale_f32 v42, s[0:1], v9, v9, 1.0
	v_rcp_f32_e32 v43, v42
	global_load_dwordx4 v[34:37], v0, s[8:9]
	global_load_dwordx4 v[38:41], v0, s[10:11]
	v_fma_f32 v44, -v42, v43, 1.0
	v_fmac_f32_e32 v43, v44, v43
	v_div_scale_f32 v44, vcc, 1.0, v9, 1.0
	v_mul_f32_e32 v45, v44, v43
	v_fma_f32 v46, -v42, v45, v44
	v_fmac_f32_e32 v45, v46, v43
	v_fma_f32 v42, -v42, v45, v44
	v_div_fmas_f32 v56, v42, v43, v45
	global_load_dwordx4 v[42:45], v0, s[8:9] offset:1024
	global_load_dwordx4 v[46:49], v0, s[10:11] offset:1024
	v_div_fixup_f32 v56, v56, v9, 1.0
	v_pk_fma_f32 v[10:11], v[56:57], v[10:11], v[14:15] op_sel_hi:[0,1,1]
	s_waitcnt vmcnt(5)
	v_pk_add_f32 v[10:11], v[10:11], v[26:27]
	v_pk_fma_f32 v[12:13], v[56:57], v[12:13], v[16:17] op_sel_hi:[0,1,1]
	v_add_f32_e32 v9, 0, v10
	v_add_f32_e32 v9, v9, v11
	v_pk_add_f32 v[12:13], v[12:13], v[28:29]
	v_pk_fma_f32 v[6:7], v[56:57], v[6:7], v[22:23] op_sel_hi:[0,1,1]
	v_add_f32_e32 v9, v9, v12
	v_pk_mul_f32 v[14:15], v[20:21], v[54:55]
	v_add_f32_e32 v9, v9, v13
	s_waitcnt vmcnt(4)
	v_pk_add_f32 v[6:7], v[6:7], v[30:31]
	v_pk_fma_f32 v[14:15], v[56:57], v[14:15], v[24:25] op_sel_hi:[0,1,1]
	v_add_f32_e32 v9, v9, v6
	v_add_f32_e32 v9, v9, v7
	v_pk_add_f32 v[14:15], v[14:15], v[32:33]
	s_nop 0
	v_add_f32_e32 v9, v9, v14
	v_add_f32_e32 v9, v9, v15
	s_nop 1
	v_add_f32_dpp v9, v9, v9 quad_perm:[1,0,3,2] row_mask:0xf bank_mask:0xf bound_ctrl:1
	s_nop 1
	v_add_f32_dpp v9, v9, v9 quad_perm:[2,3,0,1] row_mask:0xf bank_mask:0xf bound_ctrl:1
	s_nop 1
	v_add_f32_dpp v9, v9, v9 row_half_mirror row_mask:0xf bank_mask:0xf bound_ctrl:1
	s_nop 1
	v_add_f32_dpp v9, v9, v9 row_mirror row_mask:0xf bank_mask:0xf bound_ctrl:1
	s_nop 0
	v_readlane_b32 s8, v9, 16
	v_readlane_b32 s9, v9, 48
	v_readlane_b32 s0, v9, 0
	v_readlane_b32 s1, v9, 32
	v_mov_b32_e32 v16, s8
	v_mov_b32_e32 v17, s9
	v_pk_add_f32 v[16:17], s[0:1], v[16:17]
	s_nop 0
	v_add_f32_e32 v9, v16, v17
	v_mul_f32_e32 v16, 0x3b000000, v9
	v_pk_add_f32 v[10:11], v[10:11], v[16:17] op_sel_hi:[1,0] neg_lo:[0,1] neg_hi:[0,1]
	v_pk_add_f32 v[12:13], v[12:13], v[16:17] op_sel_hi:[1,0] neg_lo:[0,1] neg_hi:[0,1]
	v_pk_mul_f32 v[18:19], v[10:11], v[10:11]
	v_pk_mul_f32 v[20:21], v[12:13], v[12:13]
	v_add_f32_e32 v9, v18, v19
	v_pk_add_f32 v[22:23], v[6:7], v[16:17] op_sel_hi:[1,0] neg_lo:[0,1] neg_hi:[0,1]
	v_add_f32_e32 v9, v9, v20
	v_pk_mul_f32 v[6:7], v[22:23], v[22:23]
	v_add_f32_e32 v9, v9, v21
	v_pk_add_f32 v[14:15], v[14:15], v[16:17] op_sel_hi:[1,0] neg_lo:[0,1] neg_hi:[0,1]
	v_add_f32_e32 v6, v9, v6
	v_pk_mul_f32 v[16:17], v[14:15], v[14:15]
	v_add_f32_e32 v6, v6, v7
	v_add_f32_e32 v6, v6, v16
	v_add_f32_e32 v6, v6, v17
	s_nop 1
	v_add_f32_dpp v6, v6, v6 quad_perm:[1,0,3,2] row_mask:0xf bank_mask:0xf bound_ctrl:1
	s_nop 1
	v_add_f32_dpp v6, v6, v6 quad_perm:[2,3,0,1] row_mask:0xf bank_mask:0xf bound_ctrl:1
	s_nop 1
	v_add_f32_dpp v6, v6, v6 row_half_mirror row_mask:0xf bank_mask:0xf bound_ctrl:1
	s_nop 1
	v_add_f32_dpp v6, v6, v6 row_mirror row_mask:0xf bank_mask:0xf bound_ctrl:1
	s_nop 0
	v_readlane_b32 s8, v6, 16
	v_readlane_b32 s9, v6, 48
	v_readlane_b32 s0, v6, 0
	v_readlane_b32 s1, v6, 32
	v_mov_b32_e32 v6, s8
	v_mov_b32_e32 v7, s9
	v_pk_add_f32 v[6:7], s[0:1], v[6:7]
	s_nop 0
	v_add_f32_e32 v6, v6, v7
	v_fmac_f32_e32 v57, 0x3b000000, v6
	v_mul_f32_e32 v6, 0x4f800000, v57
	v_cmp_gt_f32_e32 vcc, s12, v57
	s_nop 1
	v_cndmask_b32_e32 v6, v57, v6, vcc
	v_sqrt_f32_e32 v7, v6
	s_nop 0
	v_add_u32_e32 v9, -1, v7
	v_fma_f32 v16, -v9, v7, v6
	v_cmp_ge_f32_e64 s[0:1], 0, v16
	v_add_u32_e32 v16, 1, v7
	s_nop 0
	v_cndmask_b32_e64 v9, v7, v9, s[0:1]
	v_fma_f32 v7, -v16, v7, v6
	v_cmp_lt_f32_e64 s[0:1], 0, v7
	s_nop 1
	v_cndmask_b32_e64 v7, v9, v16, s[0:1]
	v_mul_f32_e32 v9, 0x37800000, v7
	v_cndmask_b32_e32 v7, v7, v9, vcc
	v_cmp_class_f32_e32 vcc, v6, v58
	v_lshl_add_u64 v[16:17], v[4:5], 0, v[0:1]
	s_nop 0
	v_cndmask_b32_e32 v6, v7, v6, vcc
	v_div_scale_f32 v7, s[0:1], v6, v6, 1.0
	v_rcp_f32_e32 v9, v7
	s_mov_b32 s0, 0x43000000
	v_fma_f32 v0, -v7, v9, 1.0
	v_fmac_f32_e32 v9, v0, v9
	v_div_scale_f32 v0, vcc, 1.0, v6, 1.0
	v_mul_f32_e32 v4, v0, v9
	v_fma_f32 v5, -v7, v4, v0
	v_fmac_f32_e32 v4, v5, v9
	v_fma_f32 v0, -v7, v4, v0
	v_div_fmas_f32 v0, v0, v9, v4
	v_div_fixup_f32 v0, v0, v6, 1.0
	s_waitcnt vmcnt(3)
	v_pk_mul_f32 v[4:5], v[34:35], v[10:11]
	v_pk_mul_f32 v[6:7], v[36:37], v[12:13]
	s_waitcnt vmcnt(2)
	v_pk_fma_f32 v[4:5], v[0:1], v[4:5], v[38:39] op_sel_hi:[0,1,1]
	v_pk_fma_f32 v[6:7], v[0:1], v[6:7], v[40:41] op_sel_hi:[0,1,1]
	s_waitcnt vmcnt(1)
	v_pk_mul_f32 v[10:11], v[42:43], v[22:23]
	v_pk_mul_f32 v[12:13], v[44:45], v[14:15]
	v_fma_mixlo_f16 v9, v4, s0, 0
	s_waitcnt vmcnt(0)
	v_pk_fma_f32 v[10:11], v[0:1], v[10:11], v[46:47] op_sel_hi:[0,1,1]
	v_pk_fma_f32 v[12:13], v[0:1], v[12:13], v[48:49] op_sel_hi:[0,1,1]
	global_store_dwordx4 v[16:17], v[4:7], off sc1
	global_store_dwordx4 v[16:17], v[10:13], off offset:1024 sc1
	v_mul_f32_e32 v0, 0x43000000, v4
	v_fma_mixlo_f16 v4, v4, s0, -v9 op_sel_hi:[0,0,1]
	v_fma_mixlo_f16 v15, v5, s0, 0
	v_pk_mul_f32 v[18:19], v[6:7], s[0:1] op_sel_hi:[1,0]
	v_fma_mixhi_f16 v4, v5, s0, -v15 op_sel_hi:[0,0,1]
	v_cvt_pk_f16_f32 v15, v18, v19
	v_pk_mul_f32 v[20:21], v[12:13], s[0:1] op_sel_hi:[1,0]
	v_cvt_f32_f16_e32 v18, v15
	v_cvt_f32_f16_sdwa v19, v15 dst_sel:DWORD dst_unused:UNUSED_PAD src0_sel:WORD_1
	v_cvt_pk_f16_f32 v17, v20, v21
	v_cvt_f32_f16_e32 v20, v17
	v_cvt_f32_f16_sdwa v21, v17 dst_sel:DWORD dst_unused:UNUSED_PAD src0_sel:WORD_1
	v_fma_mixlo_f16 v14, v10, s0, 0
	v_mul_f32_e32 v9, 0x43000000, v10
	v_fma_mixlo_f16 v10, v10, s0, -v14 op_sel_hi:[0,0,1]
	v_mul_f32_e32 v14, 0x43000000, v5
	v_fma_mixlo_f16 v5, v11, s0, 0
	v_pk_fma_f32 v[6:7], v[6:7], s[0:1], v[18:19] op_sel_hi:[1,0,1] neg_lo:[0,0,1] neg_hi:[0,0,1]
	v_cvt_pk_f16_f32 v14, v0, v14
	v_mul_f32_e32 v0, 0x43000000, v11
	v_fma_mixhi_f16 v10, v11, s0, -v5 op_sel_hi:[0,0,1]
	v_cvt_pk_f16_f32 v5, v6, v7
	v_pk_fma_f32 v[6:7], v[12:13], s[0:1], v[20:21] op_sel_hi:[1,0,1] neg_lo:[0,0,1] neg_hi:[0,0,1]
	v_cvt_pk_f16_f32 v16, v9, v0
	v_cvt_pk_f16_f32 v11, v6, v7
	v_lshl_add_u64 v[6:7], s[6:7], 0, v[2:3]
	v_lshlrev_b32_e32 v0, 1, v8
	v_lshl_add_u64 v[2:3], s[2:3], 0, v[2:3]
	v_lshl_add_u64 v[6:7], v[6:7], 0, v[0:1]
	v_lshl_add_u64 v[0:1], v[2:3], 0, v[0:1]
	v_mbcnt_lo_u32_b32 v20, -1, 0
	v_mbcnt_hi_u32_b32 v20, -1, v20
	v_and_b32_e32 v20, 1, v20
	v_cmp_eq_u32_e32 vcc, 1, v20
	v_mul_u32_u24_e32 v22, 0x1f8, v20
	v_mov_b32_e32 v23, 0
	s_nop 1
	v_mov_b32_dpp v24, v14 quad_perm:[1,0,3,2] row_mask:0xf bank_mask:0xf
	v_mov_b32_dpp v25, v15 quad_perm:[1,0,3,2] row_mask:0xf bank_mask:0xf
	v_mov_b32_dpp v26, v16 quad_perm:[1,0,3,2] row_mask:0xf bank_mask:0xf
	v_mov_b32_dpp v27, v17 quad_perm:[1,0,3,2] row_mask:0xf bank_mask:0xf
	s_nop 1
	v_cndmask_b32_e32 v28, v14, v26, vcc
	v_cndmask_b32_e32 v29, v15, v27, vcc
	v_cndmask_b32_e32 v30, v24, v16, vcc
	v_cndmask_b32_e32 v31, v25, v17, vcc
	v_lshl_add_u64 v[32:33], v[6:7], 0, v[22:23]
	global_store_dwordx4 v[32:33], v[28:31], off sc1
	s_nop 1
	v_mov_b32_dpp v24, v4 quad_perm:[1,0,3,2] row_mask:0xf bank_mask:0xf
	v_mov_b32_dpp v25, v5 quad_perm:[1,0,3,2] row_mask:0xf bank_mask:0xf
	v_mov_b32_dpp v26, v10 quad_perm:[1,0,3,2] row_mask:0xf bank_mask:0xf
	v_mov_b32_dpp v27, v11 quad_perm:[1,0,3,2] row_mask:0xf bank_mask:0xf
	s_nop 1
	v_cndmask_b32_e32 v28, v4, v26, vcc
	v_cndmask_b32_e32 v29, v5, v27, vcc
	v_cndmask_b32_e32 v30, v24, v10, vcc
	v_cndmask_b32_e32 v31, v25, v11, vcc
	v_lshl_add_u64 v[32:33], v[0:1], 0, v[22:23]
	global_store_dwordx4 v[32:33], v[28:31], off sc1
	s_nop 1
	s_endpgm
	s_endpgm
	s_endpgm
	s_endpgm
	s_endpgm
	s_endpgm
	s_endpgm
	s_endpgm
	s_endpgm
	s_endpgm
	s_endpgm
	s_endpgm
	s_endpgm
	s_endpgm
	s_endpgm
	s_endpgm
	s_endpgm
	s_endpgm
	s_endpgm
	s_endpgm
	s_endpgm
	s_endpgm
	s_endpgm
	s_endpgm
	s_endpgm
	s_endpgm
	s_endpgm
	s_endpgm
	s_endpgm
	s_endpgm
	s_endpgm
	s_endpgm
	s_endpgm
	s_endpgm
	s_endpgm
	s_endpgm
	s_endpgm
	s_endpgm
	s_endpgm
	s_endpgm
	s_endpgm
	s_endpgm
	s_endpgm
	s_endpgm
	s_endpgm
	s_endpgm
	s_endpgm
	s_endpgm
	s_endpgm
	s_endpgm
	s_endpgm
	s_endpgm
	s_endpgm
	s_endpgm
	s_endpgm

.LBB19_5:
	v_lshlrev_b32_e32 v0, 2, v0
	v_and_b32_e32 v50, 0xfc, v0
	v_lshlrev_b64 v[2:3], 11, v[2:3]
	v_lshlrev_b32_e32 v4, 2, v50
	v_mov_b32_e32 v5, 0
	s_waitcnt lgkmcnt(0)
	v_lshl_add_u64 v[2:3], s[14:15], 0, v[2:3]
	v_lshlrev_b64 v[36:37], 11, v[6:7]
	v_lshl_add_u64 v[2:3], v[2:3], 0, v[4:5]
	v_lshl_add_u64 v[0:1], s[18:19], 0, v[36:37]
	global_load_dwordx4 v[8:11], v[2:3], off
	global_load_dwordx4 v[12:15], v4, s[16:17]
	global_load_dwordx4 v[16:19], v4, s[16:17] offset:1024
	global_load_dwordx4 v[20:23], v[2:3], off offset:1024
	v_lshl_add_u64 v[38:39], v[0:1], 0, v[4:5]
	global_load_dwordx4 v[24:27], v[38:39], off
	global_load_dwordx4 v[28:31], v[38:39], off offset:1024
	global_load_dwordx4 v[32:35], v4, s[4:5]
	global_load_dwordx4 v[0:3], v4, s[4:5] offset:1024
	v_lshl_add_u64 v[36:37], s[8:9], 0, v[36:37]
	v_lshl_add_u64 v[48:49], v[36:37], 0, v[4:5]
	global_load_dwordx4 v[36:39], v4, s[6:7]
	global_load_dwordx4 v[40:43], v4, s[6:7] offset:1024
	v_lshlrev_b64 v[6:7], 10, v[6:7]
	v_lshl_add_u64 v[44:45], s[10:11], 0, v[6:7]
	v_lshl_add_u64 v[46:47], s[2:3], 0, v[6:7]
	v_mov_b32_e32 v51, 0x3727c5ac
	s_mov_b32 s5, 0xf800000
	v_mov_b32_e32 v52, 0x260
	s_mov_b32 s4, 0x43000000
	v_lshlrev_b32_e32 v4, 1, v50
	v_lshl_add_u64 v[44:45], v[44:45], 0, v[4:5]
	s_waitcnt vmcnt(8)
	v_pk_add_f32 v[6:7], v[12:13], v[8:9]
	s_waitcnt vmcnt(5)
	v_pk_add_f32 v[6:7], v[24:25], v[6:7]
	v_pk_add_f32 v[8:9], v[14:15], v[10:11]
	v_add_f32_e32 v14, 0, v6
	v_pk_add_f32 v[8:9], v[26:27], v[8:9]
	v_add_f32_e32 v14, v14, v7
	v_pk_add_f32 v[10:11], v[16:17], v[20:21]
	v_add_f32_e32 v14, v14, v8
	s_waitcnt vmcnt(4)
	v_pk_add_f32 v[10:11], v[28:29], v[10:11]
	v_add_f32_e32 v14, v14, v9
	v_pk_add_f32 v[12:13], v[18:19], v[22:23]
	v_add_f32_e32 v14, v14, v10
	v_pk_add_f32 v[12:13], v[30:31], v[12:13]
	v_add_f32_e32 v14, v14, v11
	v_add_f32_e32 v14, v14, v12
	v_add_f32_e32 v14, v14, v13
	s_nop 1
	v_add_f32_dpp v14, v14, v14 quad_perm:[1,0,3,2] row_mask:0xf bank_mask:0xf bound_ctrl:1
	s_nop 1
	v_add_f32_dpp v14, v14, v14 quad_perm:[2,3,0,1] row_mask:0xf bank_mask:0xf bound_ctrl:1
	s_nop 1
	v_add_f32_dpp v14, v14, v14 row_half_mirror row_mask:0xf bank_mask:0xf bound_ctrl:1
	s_nop 1
	v_add_f32_dpp v14, v14, v14 row_mirror row_mask:0xf bank_mask:0xf bound_ctrl:1
	s_nop 0
	v_readlane_b32 s2, v14, 16
	v_readlane_b32 s3, v14, 48
	v_readlane_b32 s0, v14, 0
	v_readlane_b32 s1, v14, 32
	v_mov_b32_e32 v14, s2
	v_mov_b32_e32 v15, s3
	v_pk_add_f32 v[14:15], s[0:1], v[14:15]
	s_nop 0
	v_add_f32_e32 v14, v14, v15
	v_mul_f32_e32 v14, 0x3b000000, v14
	v_pk_add_f32 v[6:7], v[6:7], v[14:15] op_sel_hi:[1,0] neg_lo:[0,1] neg_hi:[0,1]
	v_pk_add_f32 v[8:9], v[8:9], v[14:15] op_sel_hi:[1,0] neg_lo:[0,1] neg_hi:[0,1]
	v_pk_add_f32 v[10:11], v[10:11], v[14:15] op_sel_hi:[1,0] neg_lo:[0,1] neg_hi:[0,1]
	v_pk_add_f32 v[12:13], v[12:13], v[14:15] op_sel_hi:[1,0] neg_lo:[0,1] neg_hi:[0,1]
	v_pk_mul_f32 v[14:15], v[6:7], v[6:7]
	v_pk_mul_f32 v[16:17], v[8:9], v[8:9]
	v_add_f32_e32 v14, v14, v15
	v_add_f32_e32 v14, v14, v16
	v_pk_mul_f32 v[18:19], v[10:11], v[10:11]
	v_add_f32_e32 v14, v14, v17
	v_add_f32_e32 v14, v14, v18
	v_pk_mul_f32 v[20:21], v[12:13], v[12:13]
	v_add_f32_e32 v14, v14, v19
	v_add_f32_e32 v14, v14, v20
	v_add_f32_e32 v14, v14, v21
	s_waitcnt vmcnt(2)
	v_pk_mul_f32 v[10:11], v[0:1], v[10:11]
	v_pk_mul_f32 v[12:13], v[2:3], v[12:13]
	v_add_f32_dpp v14, v14, v14 quad_perm:[1,0,3,2] row_mask:0xf bank_mask:0xf bound_ctrl:1
	v_pk_mul_f32 v[6:7], v[32:33], v[6:7]
	v_pk_mul_f32 v[8:9], v[34:35], v[8:9]
	v_add_f32_dpp v14, v14, v14 quad_perm:[2,3,0,1] row_mask:0xf bank_mask:0xf bound_ctrl:1
	s_nop 1
	v_add_f32_dpp v14, v14, v14 row_half_mirror row_mask:0xf bank_mask:0xf bound_ctrl:1
	s_nop 1
	v_add_f32_dpp v14, v14, v14 row_mirror row_mask:0xf bank_mask:0xf bound_ctrl:1
	s_nop 0
	v_readlane_b32 s2, v14, 16
	v_readlane_b32 s3, v14, 48
	v_readlane_b32 s0, v14, 0
	v_readlane_b32 s1, v14, 32
	v_mov_b32_e32 v14, s2
	v_mov_b32_e32 v15, s3
	v_pk_add_f32 v[14:15], s[0:1], v[14:15]
	s_nop 0
	v_add_f32_e32 v14, v14, v15
	v_fmac_f32_e32 v51, 0x3b000000, v14
	v_mul_f32_e32 v14, 0x4f800000, v51
	v_cmp_gt_f32_e32 vcc, s5, v51
	s_nop 1
	v_cndmask_b32_e32 v14, v51, v14, vcc
	v_sqrt_f32_e32 v15, v14
	s_nop 0
	v_add_u32_e32 v0, -1, v15
	v_add_u32_e32 v1, 1, v15
	v_fma_f32 v16, -v0, v15, v14
	v_fma_f32 v17, -v1, v15, v14
	v_cmp_ge_f32_e64 s[0:1], 0, v16
	s_nop 1
	v_cndmask_b32_e64 v0, v15, v0, s[0:1]
	v_cmp_lt_f32_e64 s[0:1], 0, v17
	s_nop 1
	v_cndmask_b32_e64 v0, v0, v1, s[0:1]
	v_mul_f32_e32 v1, 0x37800000, v0
	v_cndmask_b32_e32 v0, v0, v1, vcc
	v_cmp_class_f32_e32 vcc, v14, v52
	s_nop 1
	v_cndmask_b32_e32 v0, v0, v14, vcc
	v_div_scale_f32 v1, s[0:1], v0, v0, 1.0
	v_rcp_f32_e32 v14, v1
	v_div_scale_f32 v2, vcc, 1.0, v0, 1.0
	v_fma_f32 v3, -v1, v14, 1.0
	v_fmac_f32_e32 v14, v3, v14
	v_mul_f32_e32 v3, v2, v14
	v_fma_f32 v15, -v1, v3, v2
	v_fmac_f32_e32 v3, v15, v14
	v_fma_f32 v1, -v1, v3, v2
	v_div_fmas_f32 v1, v1, v14, v3
	v_div_fixup_f32 v14, v1, v0, 1.0
	s_waitcnt vmcnt(1)
	v_pk_fma_f32 v[0:1], v[14:15], v[6:7], v[36:37] op_sel_hi:[0,1,1]
	v_pk_fma_f32 v[2:3], v[14:15], v[8:9], v[38:39] op_sel_hi:[0,1,1]
	s_waitcnt vmcnt(0)
	v_pk_fma_f32 v[6:7], v[14:15], v[10:11], v[40:41] op_sel_hi:[0,1,1]
	v_pk_fma_f32 v[8:9], v[14:15], v[12:13], v[42:43] op_sel_hi:[0,1,1]
	v_fma_mixlo_f16 v15, v0, s4, 0
	v_pk_mul_f32 v[10:11], v[2:3], s[4:5] op_sel_hi:[1,0]
	global_store_dwordx4 v[48:49], v[0:3], off sc1
	global_store_dwordx4 v[48:49], v[6:9], off offset:1024 sc1
	v_mul_f32_e32 v14, 0x43000000, v0
	v_fma_mixlo_f16 v17, v6, s4, 0
	v_pk_mul_f32 v[12:13], v[8:9], s[4:5] op_sel_hi:[1,0]
	v_fma_mixlo_f16 v0, v0, s4, -v15 op_sel_hi:[0,0,1]
	v_cvt_pk_f16_f32 v15, v10, v11
	v_mul_f32_e32 v16, 0x43000000, v6
	v_fma_mixlo_f16 v6, v6, s4, -v17 op_sel_hi:[0,0,1]
	v_cvt_pk_f16_f32 v17, v12, v13
	v_cvt_f32_f16_e32 v10, v15
	v_cvt_f32_f16_sdwa v11, v15 dst_sel:DWORD dst_unused:UNUSED_PAD src0_sel:WORD_1
	v_cvt_f32_f16_e32 v12, v17
	v_cvt_f32_f16_sdwa v13, v17 dst_sel:DWORD dst_unused:UNUSED_PAD src0_sel:WORD_1
	v_mul_f32_e32 v18, 0x43000000, v1
	v_fma_mixlo_f16 v19, v1, s4, 0
	v_pk_fma_f32 v[2:3], v[2:3], s[4:5], v[10:11] op_sel_hi:[1,0,1] neg_lo:[0,0,1] neg_hi:[0,0,1]
	v_mul_f32_e32 v20, 0x43000000, v7
	v_fma_mixlo_f16 v21, v7, s4, 0
	v_cvt_pk_f16_f32 v14, v14, v18
	v_fma_mixhi_f16 v0, v1, s4, -v19 op_sel_hi:[0,0,1]
	v_pk_fma_f32 v[8:9], v[8:9], s[4:5], v[12:13] op_sel_hi:[1,0,1] neg_lo:[0,0,1] neg_hi:[0,0,1]
	v_cvt_pk_f16_f32 v1, v2, v3
	v_lshl_add_u64 v[2:3], v[46:47], 0, v[4:5]
	v_cvt_pk_f16_f32 v16, v16, v20
	v_fma_mixhi_f16 v6, v7, s4, -v21 op_sel_hi:[0,0,1]
	v_cvt_pk_f16_f32 v7, v8, v9
	v_mbcnt_lo_u32_b32 v20, -1, 0
	v_mbcnt_hi_u32_b32 v20, -1, v20
	v_and_b32_e32 v20, 1, v20
	v_cmp_eq_u32_e32 vcc, 1, v20
	v_mul_u32_u24_e32 v22, 0x1f8, v20
	v_mov_b32_e32 v23, 0
	s_nop 1
	v_mov_b32_dpp v24, v14 quad_perm:[1,0,3,2] row_mask:0xf bank_mask:0xf
	v_mov_b32_dpp v25, v15 quad_perm:[1,0,3,2] row_mask:0xf bank_mask:0xf
	v_mov_b32_dpp v26, v16 quad_perm:[1,0,3,2] row_mask:0xf bank_mask:0xf
	v_mov_b32_dpp v27, v17 quad_perm:[1,0,3,2] row_mask:0xf bank_mask:0xf
	s_nop 1
	v_cndmask_b32_e32 v28, v14, v26, vcc
	v_cndmask_b32_e32 v29, v15, v27, vcc
	v_cndmask_b32_e32 v30, v24, v16, vcc
	v_cndmask_b32_e32 v31, v25, v17, vcc
	v_lshl_add_u64 v[32:33], v[44:45], 0, v[22:23]
	global_store_dwordx4 v[32:33], v[28:31], off sc1
	s_nop 1
	v_mov_b32_dpp v24, v0 quad_perm:[1,0,3,2] row_mask:0xf bank_mask:0xf
	v_mov_b32_dpp v25, v1 quad_perm:[1,0,3,2] row_mask:0xf bank_mask:0xf
	v_mov_b32_dpp v26, v6 quad_perm:[1,0,3,2] row_mask:0xf bank_mask:0xf
	v_mov_b32_dpp v27, v7 quad_perm:[1,0,3,2] row_mask:0xf bank_mask:0xf
	s_nop 1
	v_cndmask_b32_e32 v28, v0, v26, vcc
	v_cndmask_b32_e32 v29, v1, v27, vcc
	v_cndmask_b32_e32 v30, v24, v6, vcc
	v_cndmask_b32_e32 v31, v25, v7, vcc
	v_lshl_add_u64 v[32:33], v[2:3], 0, v[22:23]
	global_store_dwordx4 v[32:33], v[28:31], off sc1
	s_nop 1
	s_endpgm
	s_endpgm
	s_endpgm
	s_endpgm
	s_endpgm
	s_endpgm
	s_endpgm
	s_endpgm
	s_endpgm
	s_endpgm
	s_endpgm
	s_endpgm
	s_endpgm
	s_endpgm
	s_endpgm
	s_endpgm
	s_endpgm
	s_endpgm
	s_endpgm
	s_endpgm
	s_endpgm
	s_endpgm
	s_endpgm
	s_endpgm
	s_endpgm
	s_endpgm
	s_endpgm
	s_endpgm
	s_endpgm
	s_endpgm
	s_endpgm
	s_endpgm
	s_endpgm
	s_endpgm
	s_endpgm
	s_endpgm
	s_endpgm
	s_endpgm

.LBB20_5:
	v_lshlrev_b32_e32 v0, 2, v0
	s_load_dwordx2 s[0:1], s[0:1], 0x8
	v_and_b32_e32 v54, 0xfc, v0
	v_lshlrev_b64 v[44:45], 11, v[2:3]
	v_lshlrev_b64 v[4:5], 11, v[4:5]
	s_waitcnt lgkmcnt(0)
	v_lshl_add_u64 v[24:25], s[18:19], 0, v[44:45]
	v_lshlrev_b32_e32 v0, 2, v54
	v_mov_b32_e32 v1, 0
	v_lshl_add_u64 v[4:5], s[14:15], 0, v[4:5]
	v_lshl_add_u64 v[20:21], v[4:5], 0, v[0:1]
	v_lshl_add_u64 v[26:27], v[24:25], 0, v[0:1]
	global_load_dwordx4 v[4:7], v[20:21], off
	global_load_dwordx4 v[8:11], v0, s[16:17]
	global_load_dwordx4 v[12:15], v0, s[16:17] offset:1024
	global_load_dwordx4 v[16:19], v[20:21], off offset:1024
	v_lshl_add_u64 v[28:29], s[0:1], 2, v[24:25]
	global_load_dwordx4 v[20:23], v[26:27], off
	v_lshl_add_u64 v[46:47], v[28:29], 0, v[0:1]
	global_load_dwordx4 v[24:27], v[26:27], off offset:1024
	s_nop 0
	global_load_dwordx4 v[28:31], v[46:47], off
	global_load_dwordx4 v[32:35], v[46:47], off offset:1024
	global_load_dwordx4 v[36:39], v0, s[8:9]
	global_load_dwordx4 v[40:43], v0, s[8:9] offset:1024
	v_lshl_add_u64 v[44:45], s[4:5], 0, v[44:45]
	v_lshl_add_u64 v[52:53], v[44:45], 0, v[0:1]
	global_load_dwordx4 v[44:47], v0, s[10:11]
	global_load_dwordx4 v[48:51], v0, s[10:11] offset:1024
	v_mov_b32_e32 v55, 0x3727c5ac
	s_mov_b32 s9, 0xf800000
	v_mov_b32_e32 v56, 0x260
	s_mov_b32 s8, 0x43000000
	v_lshlrev_b64 v[2:3], 10, v[2:3]
	s_waitcnt vmcnt(10)
	v_pk_add_f32 v[4:5], v[8:9], v[4:5]
	v_pk_add_f32 v[6:7], v[10:11], v[6:7]
	s_waitcnt vmcnt(8)
	v_pk_add_f32 v[8:9], v[12:13], v[16:17]
	v_pk_add_f32 v[10:11], v[14:15], v[18:19]
	s_waitcnt vmcnt(7)
	v_pk_add_f32 v[4:5], v[4:5], v[20:21]
	v_pk_add_f32 v[6:7], v[6:7], v[22:23]
	s_waitcnt vmcnt(5)
	v_pk_add_f32 v[4:5], v[4:5], v[28:29]
	v_pk_add_f32 v[6:7], v[6:7], v[30:31]
	v_add_f32_e32 v0, 0, v4
	v_add_f32_e32 v0, v0, v5
	v_pk_add_f32 v[8:9], v[8:9], v[24:25]
	v_add_f32_e32 v0, v0, v6
	s_waitcnt vmcnt(4)
	v_pk_add_f32 v[8:9], v[8:9], v[32:33]
	v_add_f32_e32 v0, v0, v7
	v_pk_add_f32 v[10:11], v[10:11], v[26:27]
	v_add_f32_e32 v0, v0, v8
	v_pk_add_f32 v[10:11], v[10:11], v[34:35]
	v_add_f32_e32 v0, v0, v9
	v_add_f32_e32 v0, v0, v10
	v_add_f32_e32 v0, v0, v11
	s_nop 1
	v_add_f32_dpp v0, v0, v0 quad_perm:[1,0,3,2] row_mask:0xf bank_mask:0xf bound_ctrl:1
	s_nop 1
	v_add_f32_dpp v0, v0, v0 quad_perm:[2,3,0,1] row_mask:0xf bank_mask:0xf bound_ctrl:1
	s_nop 1
	v_add_f32_dpp v0, v0, v0 row_half_mirror row_mask:0xf bank_mask:0xf bound_ctrl:1
	s_nop 1
	v_add_f32_dpp v0, v0, v0 row_mirror row_mask:0xf bank_mask:0xf bound_ctrl:1
	s_nop 0
	v_readlane_b32 s4, v0, 16
	v_readlane_b32 s5, v0, 48
	v_readlane_b32 s0, v0, 0
	v_readlane_b32 s1, v0, 32
	v_mov_b32_e32 v12, s4
	v_mov_b32_e32 v13, s5
	v_pk_add_f32 v[12:13], s[0:1], v[12:13]
	s_nop 0
	v_add_f32_e32 v0, v12, v13
	v_mul_f32_e32 v0, 0x3b000000, v0
	v_pk_add_f32 v[4:5], v[4:5], v[0:1] op_sel_hi:[1,0] neg_lo:[0,1] neg_hi:[0,1]
	v_pk_add_f32 v[6:7], v[6:7], v[0:1] op_sel_hi:[1,0] neg_lo:[0,1] neg_hi:[0,1]
	v_pk_mul_f32 v[12:13], v[4:5], v[4:5]
	v_pk_add_f32 v[8:9], v[8:9], v[0:1] op_sel_hi:[1,0] neg_lo:[0,1] neg_hi:[0,1]
	v_pk_add_f32 v[10:11], v[10:11], v[0:1] op_sel_hi:[1,0] neg_lo:[0,1] neg_hi:[0,1]
	v_pk_mul_f32 v[14:15], v[6:7], v[6:7]
	v_add_f32_e32 v0, v12, v13
	v_add_f32_e32 v0, v0, v14
	v_pk_mul_f32 v[16:17], v[8:9], v[8:9]
	v_add_f32_e32 v0, v0, v15
	v_add_f32_e32 v0, v0, v16
	v_pk_mul_f32 v[18:19], v[10:11], v[10:11]
	v_add_f32_e32 v0, v0, v17
	v_add_f32_e32 v0, v0, v18
	v_add_f32_e32 v0, v0, v19
	s_waitcnt vmcnt(3)
	v_pk_mul_f32 v[6:7], v[38:39], v[6:7]
	s_waitcnt vmcnt(2)
	v_pk_mul_f32 v[8:9], v[40:41], v[8:9]
	v_add_f32_dpp v0, v0, v0 quad_perm:[1,0,3,2] row_mask:0xf bank_mask:0xf bound_ctrl:1
	v_pk_mul_f32 v[4:5], v[36:37], v[4:5]
	v_pk_mul_f32 v[10:11], v[42:43], v[10:11]
	v_add_f32_dpp v0, v0, v0 quad_perm:[2,3,0,1] row_mask:0xf bank_mask:0xf bound_ctrl:1
	s_nop 1
	v_add_f32_dpp v0, v0, v0 row_half_mirror row_mask:0xf bank_mask:0xf bound_ctrl:1
	s_nop 1
	v_add_f32_dpp v0, v0, v0 row_mirror row_mask:0xf bank_mask:0xf bound_ctrl:1
	s_nop 0
	v_readlane_b32 s4, v0, 16
	v_readlane_b32 s5, v0, 48
	v_readlane_b32 s0, v0, 0
	v_readlane_b32 s1, v0, 32
	v_mov_b32_e32 v12, s4
	v_mov_b32_e32 v13, s5
	v_pk_add_f32 v[12:13], s[0:1], v[12:13]
	s_nop 0
	v_add_f32_e32 v0, v12, v13
	v_fmac_f32_e32 v55, 0x3b000000, v0
	v_mul_f32_e32 v0, 0x4f800000, v55
	v_cmp_gt_f32_e32 vcc, s9, v55
	s_nop 1
	v_cndmask_b32_e32 v0, v55, v0, vcc
	v_sqrt_f32_e32 v12, v0
	s_nop 0
	v_add_u32_e32 v13, -1, v12
	v_add_u32_e32 v14, 1, v12
	v_fma_f32 v15, -v13, v12, v0
	v_fma_f32 v16, -v14, v12, v0
	v_cmp_ge_f32_e64 s[0:1], 0, v15
	s_nop 1
	v_cndmask_b32_e64 v12, v12, v13, s[0:1]
	v_cmp_lt_f32_e64 s[0:1], 0, v16
	s_nop 1
	v_cndmask_b32_e64 v12, v12, v14, s[0:1]
	v_mul_f32_e32 v13, 0x37800000, v12
	v_cndmask_b32_e32 v12, v12, v13, vcc
	v_cmp_class_f32_e32 vcc, v0, v56
	s_nop 1
	v_cndmask_b32_e32 v0, v12, v0, vcc
	v_div_scale_f32 v12, s[0:1], v0, v0, 1.0
	v_rcp_f32_e32 v13, v12
	v_div_scale_f32 v14, vcc, 1.0, v0, 1.0
	v_fma_f32 v15, -v12, v13, 1.0
	v_fmac_f32_e32 v13, v15, v13
	v_mul_f32_e32 v15, v14, v13
	v_fma_f32 v16, -v12, v15, v14
	v_fmac_f32_e32 v15, v16, v13
	v_fma_f32 v12, -v12, v15, v14
	v_div_fmas_f32 v12, v12, v13, v15
	v_div_fixup_f32 v0, v12, v0, 1.0
	s_waitcnt vmcnt(1)
	v_pk_fma_f32 v[6:7], v[0:1], v[6:7], v[46:47] op_sel_hi:[0,1,1]
	s_waitcnt vmcnt(0)
	v_pk_fma_f32 v[8:9], v[0:1], v[8:9], v[48:49] op_sel_hi:[0,1,1]
	v_pk_fma_f32 v[4:5], v[0:1], v[4:5], v[44:45] op_sel_hi:[0,1,1]
	v_mul_f32_e32 v17, 0x43000000, v8
	v_fma_mixlo_f16 v18, v8, s8, 0
	v_mul_f32_e32 v21, 0x43000000, v9
	v_pk_mul_f32 v[12:13], v[6:7], s[8:9] op_sel_hi:[1,0]
	v_pk_fma_f32 v[10:11], v[0:1], v[10:11], v[50:51] op_sel_hi:[0,1,1]
	global_store_dwordx4 v[52:53], v[4:7], off sc1
	global_store_dwordx4 v[52:53], v[8:11], off offset:1024 sc1
	v_mul_f32_e32 v0, 0x43000000, v4
	v_fma_mixlo_f16 v16, v4, s8, 0
	v_fma_mixlo_f16 v8, v8, s8, -v18 op_sel_hi:[0,0,1]
	v_cvt_pk_f16_f32 v18, v17, v21
	v_cvt_pk_f16_f32 v17, v12, v13
	v_mul_f32_e32 v19, 0x43000000, v5
	v_pk_mul_f32 v[14:15], v[10:11], s[8:9] op_sel_hi:[1,0]
	v_cvt_f32_f16_e32 v12, v17
	v_cvt_f32_f16_sdwa v13, v17 dst_sel:DWORD dst_unused:UNUSED_PAD src0_sel:WORD_1
	v_fma_mixlo_f16 v4, v4, s8, -v16 op_sel_hi:[0,0,1]
	v_cvt_pk_f16_f32 v16, v0, v19
	v_cvt_pk_f16_f32 v19, v14, v15
	v_cvt_f32_f16_e32 v14, v19
	v_cvt_f32_f16_sdwa v15, v19 dst_sel:DWORD dst_unused:UNUSED_PAD src0_sel:WORD_1
	v_fma_mixlo_f16 v20, v5, s8, 0
	v_pk_fma_f32 v[6:7], v[6:7], s[8:9], v[12:13] op_sel_hi:[1,0,1] neg_lo:[0,0,1] neg_hi:[0,0,1]
	v_fma_mixhi_f16 v4, v5, s8, -v20 op_sel_hi:[0,0,1]
	v_cvt_pk_f16_f32 v5, v6, v7
	v_lshl_add_u64 v[6:7], s[6:7], 0, v[2:3]
	v_lshlrev_b32_e32 v0, 1, v54
	v_lshl_add_u64 v[2:3], s[2:3], 0, v[2:3]
	v_fma_mixlo_f16 v22, v9, s8, 0
	v_pk_fma_f32 v[10:11], v[10:11], s[8:9], v[14:15] op_sel_hi:[1,0,1] neg_lo:[0,0,1] neg_hi:[0,0,1]
	v_lshl_add_u64 v[6:7], v[6:7], 0, v[0:1]
	v_lshl_add_u64 v[0:1], v[2:3], 0, v[0:1]
	v_fma_mixhi_f16 v8, v9, s8, -v22 op_sel_hi:[0,0,1]
	v_cvt_pk_f16_f32 v9, v10, v11
	v_mbcnt_lo_u32_b32 v20, -1, 0
	v_mbcnt_hi_u32_b32 v20, -1, v20
	v_and_b32_e32 v20, 1, v20
	v_cmp_eq_u32_e32 vcc, 1, v20
	v_mul_u32_u24_e32 v22, 0x1f8, v20
	v_mov_b32_e32 v23, 0
	s_nop 1
	v_mov_b32_dpp v24, v16 quad_perm:[1,0,3,2] row_mask:0xf bank_mask:0xf
	v_mov_b32_dpp v25, v17 quad_perm:[1,0,3,2] row_mask:0xf bank_mask:0xf
	v_mov_b32_dpp v26, v18 quad_perm:[1,0,3,2] row_mask:0xf bank_mask:0xf
	v_mov_b32_dpp v27, v19 quad_perm:[1,0,3,2] row_mask:0xf bank_mask:0xf
	s_nop 1
	v_cndmask_b32_e32 v28, v16, v26, vcc
	v_cndmask_b32_e32 v29, v17, v27, vcc
	v_cndmask_b32_e32 v30, v24, v18, vcc
	v_cndmask_b32_e32 v31, v25, v19, vcc
	v_lshl_add_u64 v[32:33], v[6:7], 0, v[22:23]
	global_store_dwordx4 v[32:33], v[28:31], off sc1
	s_nop 1
	v_mov_b32_dpp v24, v4 quad_perm:[1,0,3,2] row_mask:0xf bank_mask:0xf
	v_mov_b32_dpp v25, v5 quad_perm:[1,0,3,2] row_mask:0xf bank_mask:0xf
	v_mov_b32_dpp v26, v8 quad_perm:[1,0,3,2] row_mask:0xf bank_mask:0xf
	v_mov_b32_dpp v27, v9 quad_perm:[1,0,3,2] row_mask:0xf bank_mask:0xf
	s_nop 1
	v_cndmask_b32_e32 v28, v4, v26, vcc
	v_cndmask_b32_e32 v29, v5, v27, vcc
	v_cndmask_b32_e32 v30, v24, v8, vcc
	v_cndmask_b32_e32 v31, v25, v9, vcc
	v_lshl_add_u64 v[32:33], v[0:1], 0, v[22:23]
	global_store_dwordx4 v[32:33], v[28:31], off sc1
	s_nop 1
	s_endpgm
	s_endpgm
	s_endpgm
	s_endpgm
	s_endpgm
	s_endpgm
	s_endpgm
	s_endpgm
	s_endpgm
	s_endpgm
	s_endpgm
	s_endpgm
	s_endpgm
	s_endpgm
	s_endpgm
	s_endpgm

.LBB21_5:
	v_lshlrev_b32_e32 v0, 2, v0
	v_and_b32_e32 v58, 0xfc, v0
	v_lshlrev_b64 v[4:5], 11, v[4:5]
	v_lshlrev_b32_e32 v0, 2, v58
	v_mov_b32_e32 v1, 0
	s_waitcnt lgkmcnt(0)
	v_lshl_add_u64 v[4:5], s[18:19], 0, v[4:5]
	v_lshl_add_u64 v[20:21], v[4:5], 0, v[0:1]
	global_load_dwordx4 v[4:7], v[20:21], off
	global_load_dwordx4 v[8:11], v0, s[16:17]
	global_load_dwordx4 v[12:15], v0, s[16:17] offset:1024
	global_load_dwordx4 v[16:19], v[20:21], off offset:1024
	s_load_dwordx2 s[0:1], s[0:1], 0x8
	v_lshlrev_b64 v[52:53], 11, v[2:3]
	v_lshl_add_u64 v[28:29], s[14:15], 0, v[52:53]
	v_lshl_add_u64 v[24:25], v[28:29], 0, v[0:1]
	v_mov_b32_e32 v59, 0x3727c5ac
	s_waitcnt lgkmcnt(0)
	v_lshl_add_u64 v[20:21], s[0:1], 2, v[28:29]
	v_lshl_add_u64 v[26:27], s[0:1], 3, v[28:29]
	v_lshl_add_u64 v[36:37], v[20:21], 0, v[0:1]
	global_load_dwordx4 v[20:23], v[24:25], off
	v_lshl_add_u64 v[40:41], v[26:27], 0, v[0:1]
	global_load_dwordx4 v[24:27], v[24:25], off offset:1024
	v_mad_u64_u32 v[44:45], s[12:13], s0, 12, v[28:29]
	v_mov_b32_e32 v38, v45
	v_mad_u64_u32 v[42:43], s[0:1], s1, 12, v[38:39]
	global_load_dwordx4 v[28:31], v[36:37], off
	global_load_dwordx4 v[32:35], v[36:37], off offset:1024
	v_mov_b32_e32 v45, v42
	global_load_dwordx4 v[36:39], v[40:41], off
	v_lshl_add_u64 v[54:55], v[44:45], 0, v[0:1]
	global_load_dwordx4 v[40:43], v[40:41], off offset:1024
	s_nop 0
	global_load_dwordx4 v[44:47], v[54:55], off
	global_load_dwordx4 v[48:51], v[54:55], off offset:1024
	v_mov_b32_e32 v60, 0x260
	v_lshlrev_b64 v[2:3], 10, v[2:3]
	s_waitcnt vmcnt(10)
	v_pk_add_f32 v[54:55], v[8:9], v[4:5]
	v_pk_add_f32 v[56:57], v[10:11], v[6:7]
	global_load_dwordx4 v[4:7], v0, s[8:9]
	global_load_dwordx4 v[8:11], v0, s[8:9] offset:1024
	s_waitcnt vmcnt(10)
	v_pk_add_f32 v[16:17], v[12:13], v[16:17]
	v_lshl_add_u64 v[12:13], s[4:5], 0, v[52:53]
	v_pk_add_f32 v[18:19], v[14:15], v[18:19]
	v_lshl_add_u64 v[52:53], v[12:13], 0, v[0:1]
	global_load_dwordx4 v[12:15], v0, s[10:11]
	s_mov_b32 s9, 0xf800000
	s_mov_b32 s8, 0x43000000
	s_waitcnt vmcnt(10)
	v_pk_add_f32 v[20:21], v[54:55], v[20:21]
	v_pk_add_f32 v[22:23], v[56:57], v[22:23]
	s_waitcnt vmcnt(9)
	v_pk_add_f32 v[24:25], v[16:17], v[24:25]
	v_pk_add_f32 v[26:27], v[18:19], v[26:27]
	global_load_dwordx4 v[16:19], v0, s[10:11] offset:1024
	s_waitcnt vmcnt(9)
	v_pk_add_f32 v[20:21], v[20:21], v[28:29]
	v_pk_add_f32 v[22:23], v[22:23], v[30:31]
	s_waitcnt vmcnt(8)
	v_pk_add_f32 v[24:25], v[24:25], v[32:33]
	s_waitcnt vmcnt(7)
	v_pk_add_f32 v[20:21], v[20:21], v[36:37]
	v_pk_add_f32 v[22:23], v[22:23], v[38:39]
	s_waitcnt vmcnt(5)
	v_pk_add_f32 v[20:21], v[20:21], v[44:45]
	v_pk_add_f32 v[22:23], v[22:23], v[46:47]
	v_add_f32_e32 v0, 0, v20
	v_add_f32_e32 v0, v0, v21
	v_pk_add_f32 v[24:25], v[24:25], v[40:41]
	v_add_f32_e32 v0, v0, v22
	v_pk_add_f32 v[26:27], v[26:27], v[34:35]
	s_waitcnt vmcnt(4)
	v_pk_add_f32 v[24:25], v[24:25], v[48:49]
	v_add_f32_e32 v0, v0, v23
	v_pk_add_f32 v[26:27], v[26:27], v[42:43]
	v_add_f32_e32 v0, v0, v24
	v_pk_add_f32 v[26:27], v[26:27], v[50:51]
	v_add_f32_e32 v0, v0, v25
	v_add_f32_e32 v0, v0, v26
	v_add_f32_e32 v0, v0, v27
	s_nop 1
	v_add_f32_dpp v0, v0, v0 quad_perm:[1,0,3,2] row_mask:0xf bank_mask:0xf bound_ctrl:1
	s_nop 1
	v_add_f32_dpp v0, v0, v0 quad_perm:[2,3,0,1] row_mask:0xf bank_mask:0xf bound_ctrl:1
	s_nop 1
	v_add_f32_dpp v0, v0, v0 row_half_mirror row_mask:0xf bank_mask:0xf bound_ctrl:1
	s_nop 1
	v_add_f32_dpp v0, v0, v0 row_mirror row_mask:0xf bank_mask:0xf bound_ctrl:1
	s_nop 0
	v_readlane_b32 s4, v0, 16
	v_readlane_b32 s5, v0, 48
	v_readlane_b32 s0, v0, 0
	v_readlane_b32 s1, v0, 32
	v_mov_b32_e32 v28, s4
	v_mov_b32_e32 v29, s5
	v_pk_add_f32 v[28:29], s[0:1], v[28:29]
	s_nop 0
	v_add_f32_e32 v0, v28, v29
	v_mul_f32_e32 v0, 0x3b000000, v0
	v_pk_add_f32 v[20:21], v[20:21], v[0:1] op_sel_hi:[1,0] neg_lo:[0,1] neg_hi:[0,1]
	v_pk_add_f32 v[22:23], v[22:23], v[0:1] op_sel_hi:[1,0] neg_lo:[0,1] neg_hi:[0,1]
	v_pk_mul_f32 v[28:29], v[20:21], v[20:21]
	v_pk_add_f32 v[24:25], v[24:25], v[0:1] op_sel_hi:[1,0] neg_lo:[0,1] neg_hi:[0,1]
	v_pk_add_f32 v[26:27], v[26:27], v[0:1] op_sel_hi:[1,0] neg_lo:[0,1] neg_hi:[0,1]
	v_pk_mul_f32 v[30:31], v[22:23], v[22:23]
	v_add_f32_e32 v0, v28, v29
	v_add_f32_e32 v0, v0, v30
	v_pk_mul_f32 v[32:33], v[24:25], v[24:25]
	v_add_f32_e32 v0, v0, v31
	v_add_f32_e32 v0, v0, v32
	v_pk_mul_f32 v[34:35], v[26:27], v[26:27]
	v_add_f32_e32 v0, v0, v33
	v_add_f32_e32 v0, v0, v34
	v_add_f32_e32 v0, v0, v35
	s_waitcnt vmcnt(3)
	v_pk_mul_f32 v[4:5], v[4:5], v[20:21]
	v_add_f32_dpp v0, v0, v0 quad_perm:[1,0,3,2] row_mask:0xf bank_mask:0xf bound_ctrl:1
	v_pk_mul_f32 v[6:7], v[6:7], v[22:23]
	s_waitcnt vmcnt(2)
	v_pk_mul_f32 v[8:9], v[8:9], v[24:25]
	v_add_f32_dpp v0, v0, v0 quad_perm:[2,3,0,1] row_mask:0xf bank_mask:0xf bound_ctrl:1
	v_pk_mul_f32 v[10:11], v[10:11], v[26:27]
	s_nop 0
	v_add_f32_dpp v0, v0, v0 row_half_mirror row_mask:0xf bank_mask:0xf bound_ctrl:1
	s_nop 1
	v_add_f32_dpp v0, v0, v0 row_mirror row_mask:0xf bank_mask:0xf bound_ctrl:1
	s_nop 0
	v_readlane_b32 s4, v0, 16
	v_readlane_b32 s5, v0, 48
	v_readlane_b32 s0, v0, 0
	v_readlane_b32 s1, v0, 32
	v_mov_b32_e32 v28, s4
	v_mov_b32_e32 v29, s5
	v_pk_add_f32 v[28:29], s[0:1], v[28:29]
	s_nop 0
	v_add_f32_e32 v0, v28, v29
	v_fmac_f32_e32 v59, 0x3b000000, v0
	v_mul_f32_e32 v0, 0x4f800000, v59
	v_cmp_gt_f32_e32 vcc, s9, v59
	s_nop 1
	v_cndmask_b32_e32 v0, v59, v0, vcc
	v_sqrt_f32_e32 v28, v0
	s_nop 0
	v_add_u32_e32 v20, -1, v28
	v_add_u32_e32 v21, 1, v28
	v_fma_f32 v22, -v20, v28, v0
	v_fma_f32 v23, -v21, v28, v0
	v_cmp_ge_f32_e64 s[0:1], 0, v22
	s_nop 1
	v_cndmask_b32_e64 v20, v28, v20, s[0:1]
	v_cmp_lt_f32_e64 s[0:1], 0, v23
	s_nop 1
	v_cndmask_b32_e64 v20, v20, v21, s[0:1]
	v_mul_f32_e32 v21, 0x37800000, v20
	v_cndmask_b32_e32 v20, v20, v21, vcc
	v_cmp_class_f32_e32 vcc, v0, v60
	s_nop 1
	v_cndmask_b32_e32 v0, v20, v0, vcc
	v_div_scale_f32 v20, s[0:1], v0, v0, 1.0
	v_rcp_f32_e32 v21, v20
	v_div_scale_f32 v22, vcc, 1.0, v0, 1.0
	v_fma_f32 v23, -v20, v21, 1.0
	v_fmac_f32_e32 v21, v23, v21
	v_mul_f32_e32 v23, v22, v21
	v_fma_f32 v24, -v20, v23, v22
	v_fmac_f32_e32 v23, v24, v21
	v_fma_f32 v20, -v20, v23, v22
	v_div_fmas_f32 v20, v20, v21, v23
	v_div_fixup_f32 v0, v20, v0, 1.0
	s_waitcnt vmcnt(1)
	v_pk_fma_f32 v[4:5], v[0:1], v[4:5], v[12:13] op_sel_hi:[0,1,1]
	v_pk_fma_f32 v[6:7], v[0:1], v[6:7], v[14:15] op_sel_hi:[0,1,1]
	s_waitcnt vmcnt(0)
	v_pk_fma_f32 v[8:9], v[0:1], v[8:9], v[16:17] op_sel_hi:[0,1,1]
	v_fma_mixlo_f16 v12, v4, s8, 0
	v_pk_fma_f32 v[10:11], v[0:1], v[10:11], v[18:19] op_sel_hi:[0,1,1]
	global_store_dwordx4 v[52:53], v[4:7], off sc1
	global_store_dwordx4 v[52:53], v[8:11], off offset:1024 sc1
	v_mul_f32_e32 v0, 0x43000000, v4
	v_fma_mixlo_f16 v4, v4, s8, -v12 op_sel_hi:[0,0,1]
	v_fma_mixlo_f16 v12, v8, s8, 0
	v_mul_f32_e32 v13, 0x43000000, v8
	v_fma_mixlo_f16 v8, v8, s8, -v12 op_sel_hi:[0,0,1]
	v_mul_f32_e32 v12, 0x43000000, v5
	v_fma_mixlo_f16 v14, v5, s8, 0
	v_cvt_pk_f16_f32 v12, v0, v12
	v_mul_f32_e32 v0, 0x43000000, v9
	v_pk_mul_f32 v[16:17], v[6:7], s[8:9] op_sel_hi:[1,0]
	v_fma_mixhi_f16 v4, v5, s8, -v14 op_sel_hi:[0,0,1]
	v_cvt_pk_f16_f32 v14, v13, v0
	v_cvt_pk_f16_f32 v13, v16, v17
	v_pk_mul_f32 v[18:19], v[10:11], s[8:9] op_sel_hi:[1,0]
	v_cvt_f32_f16_e32 v16, v13
	v_cvt_f32_f16_sdwa v17, v13 dst_sel:DWORD dst_unused:UNUSED_PAD src0_sel:WORD_1
	v_cvt_pk_f16_f32 v15, v18, v19
	v_cvt_f32_f16_e32 v18, v15
	v_cvt_f32_f16_sdwa v19, v15 dst_sel:DWORD dst_unused:UNUSED_PAD src0_sel:WORD_1
	v_fma_mixlo_f16 v5, v9, s8, 0
	v_pk_fma_f32 v[6:7], v[6:7], s[8:9], v[16:17] op_sel_hi:[1,0,1] neg_lo:[0,0,1] neg_hi:[0,0,1]
	v_fma_mixhi_f16 v8, v9, s8, -v5 op_sel_hi:[0,0,1]
	v_cvt_pk_f16_f32 v5, v6, v7
	v_pk_fma_f32 v[6:7], v[10:11], s[8:9], v[18:19] op_sel_hi:[1,0,1] neg_lo:[0,0,1] neg_hi:[0,0,1]
	v_lshlrev_b32_e32 v0, 1, v58
	v_cvt_pk_f16_f32 v9, v6, v7
	v_lshl_add_u64 v[6:7], s[6:7], 0, v[2:3]
	v_lshl_add_u64 v[2:3], s[2:3], 0, v[2:3]
	v_lshl_add_u64 v[6:7], v[6:7], 0, v[0:1]
	v_lshl_add_u64 v[0:1], v[2:3], 0, v[0:1]
	v_mbcnt_lo_u32_b32 v20, -1, 0
	v_mbcnt_hi_u32_b32 v20, -1, v20
	v_and_b32_e32 v20, 1, v20
	v_cmp_eq_u32_e32 vcc, 1, v20
	v_mul_u32_u24_e32 v22, 0x1f8, v20
	v_mov_b32_e32 v23, 0
	s_nop 1
	v_mov_b32_dpp v24, v12 quad_perm:[1,0,3,2] row_mask:0xf bank_mask:0xf
	v_mov_b32_dpp v25, v13 quad_perm:[1,0,3,2] row_mask:0xf bank_mask:0xf
	v_mov_b32_dpp v26, v14 quad_perm:[1,0,3,2] row_mask:0xf bank_mask:0xf
	v_mov_b32_dpp v27, v15 quad_perm:[1,0,3,2] row_mask:0xf bank_mask:0xf
	s_nop 1
	v_cndmask_b32_e32 v28, v12, v26, vcc
	v_cndmask_b32_e32 v29, v13, v27, vcc
	v_cndmask_b32_e32 v30, v24, v14, vcc
	v_cndmask_b32_e32 v31, v25, v15, vcc
	v_lshl_add_u64 v[32:33], v[6:7], 0, v[22:23]
	global_store_dwordx4 v[32:33], v[28:31], off sc1
	s_nop 1
	v_mov_b32_dpp v24, v4 quad_perm:[1,0,3,2] row_mask:0xf bank_mask:0xf
	v_mov_b32_dpp v25, v5 quad_perm:[1,0,3,2] row_mask:0xf bank_mask:0xf
	v_mov_b32_dpp v26, v8 quad_perm:[1,0,3,2] row_mask:0xf bank_mask:0xf
	v_mov_b32_dpp v27, v9 quad_perm:[1,0,3,2] row_mask:0xf bank_mask:0xf
	s_nop 1
	v_cndmask_b32_e32 v28, v4, v26, vcc
	v_cndmask_b32_e32 v29, v5, v27, vcc
	v_cndmask_b32_e32 v30, v24, v8, vcc
	v_cndmask_b32_e32 v31, v25, v9, vcc
	v_lshl_add_u64 v[32:33], v[0:1], 0, v[22:23]
	global_store_dwordx4 v[32:33], v[28:31], off sc1
	s_nop 1
	s_endpgm
	s_endpgm
	s_endpgm
	s_endpgm
	s_endpgm
	s_endpgm
	s_endpgm
	s_endpgm
	s_endpgm
	s_endpgm
	s_endpgm
	s_endpgm
	s_endpgm
	s_endpgm
	s_endpgm
	s_endpgm
	s_endpgm
	s_endpgm
	s_endpgm
	s_endpgm
	s_endpgm
	s_endpgm
	s_endpgm
	s_endpgm
	s_endpgm
	s_endpgm
	s_endpgm
	s_endpgm
	s_endpgm
	s_endpgm
	s_endpgm
	s_endpgm
	s_endpgm
	s_endpgm
	s_endpgm
	s_endpgm
	s_endpgm
	s_endpgm
	s_endpgm

.LBB22_5:
	v_lshlrev_b32_e32 v0, 2, v0
	v_and_b32_e32 v66, 0xfc, v0
	v_lshlrev_b64 v[4:5], 11, v[4:5]
	v_lshlrev_b32_e32 v0, 2, v66
	v_mov_b32_e32 v1, 0
	s_waitcnt lgkmcnt(0)
	v_lshl_add_u64 v[4:5], s[18:19], 0, v[4:5]
	v_lshl_add_u64 v[20:21], v[4:5], 0, v[0:1]
	global_load_dwordx4 v[4:7], v[20:21], off
	global_load_dwordx4 v[8:11], v0, s[16:17]
	global_load_dwordx4 v[12:15], v0, s[16:17] offset:1024
	global_load_dwordx4 v[16:19], v[20:21], off offset:1024
	v_lshlrev_b64 v[48:49], 11, v[2:3]
	v_lshl_add_u64 v[40:41], s[14:15], 0, v[48:49]
	v_lshl_add_u64 v[28:29], v[40:41], 0, v[0:1]
	global_load_dwordx4 v[20:23], v[28:29], off
	global_load_dwordx4 v[24:27], v[28:29], off offset:1024
	s_load_dwordx2 s[0:1], s[0:1], 0x8
	v_lshlrev_b64 v[2:3], 10, v[2:3]
	s_waitcnt lgkmcnt(0)
	v_lshl_add_u64 v[28:29], s[0:1], 2, v[40:41]
	v_lshl_add_u64 v[42:43], v[28:29], 0, v[0:1]
	v_mad_u64_u32 v[36:37], s[12:13], s0, 12, v[40:41]
	v_lshl_add_u64 v[32:33], s[0:1], 3, v[40:41]
	global_load_dwordx4 v[28:31], v[42:43], off
	v_mov_b32_e32 v38, v37
	v_lshl_add_u64 v[44:45], v[32:33], 0, v[0:1]
	v_mad_u64_u32 v[38:39], s[12:13], s1, 12, v[38:39]
	global_load_dwordx4 v[32:35], v[44:45], off
	v_mov_b32_e32 v37, v38
	v_lshl_add_u64 v[46:47], v[36:37], 0, v[0:1]
	global_load_dwordx4 v[36:39], v[46:47], off
	v_mad_u64_u32 v[52:53], s[12:13], s0, 20, v[40:41]
	v_mad_u64_u32 v[54:55], s[12:13], s0, 24, v[40:41]
	v_lshl_add_u64 v[50:51], s[0:1], 4, v[40:41]
	v_mad_u64_u32 v[40:41], s[12:13], s0, 28, v[40:41]
	v_lshl_add_u64 v[50:51], v[50:51], 0, v[0:1]
	s_waitcnt vmcnt(7)
	v_pk_add_f32 v[56:57], v[8:9], v[4:5]
	v_mov_b32_e32 v4, v53
	v_pk_add_f32 v[58:59], v[10:11], v[6:7]
	v_mov_b32_e32 v6, v55
	v_mad_u64_u32 v[10:11], s[12:13], s1, 20, v[4:5]
	s_waitcnt vmcnt(5)
	v_pk_add_f32 v[60:61], v[12:13], v[16:17]
	v_mov_b32_e32 v8, v41
	v_mad_u64_u32 v[12:13], s[12:13], s1, 24, v[6:7]
	v_mov_b32_e32 v53, v10
	v_pk_add_f32 v[62:63], v[14:15], v[18:19]
	v_mad_u64_u32 v[14:15], s[0:1], s1, 28, v[8:9]
	global_load_dwordx4 v[4:7], v[50:51], off
	v_mov_b32_e32 v55, v12
	v_lshl_add_u64 v[52:53], v[52:53], 0, v[0:1]
	v_mov_b32_e32 v41, v14
	v_lshl_add_u64 v[54:55], v[54:55], 0, v[0:1]
	global_load_dwordx4 v[12:15], v[52:53], off
	v_lshl_add_u64 v[64:65], v[40:41], 0, v[0:1]
	global_load_dwordx4 v[16:19], v[54:55], off
	global_load_dwordx4 v[8:11], v[42:43], off offset:1024
	s_waitcnt vmcnt(8)
	v_pk_add_f32 v[40:41], v[56:57], v[20:21]
	v_pk_add_f32 v[42:43], v[58:59], v[22:23]
	global_load_dwordx4 v[20:23], v[64:65], off
	s_waitcnt vmcnt(8)
	v_pk_add_f32 v[56:57], v[60:61], v[24:25]
	v_pk_add_f32 v[58:59], v[62:63], v[26:27]
	s_waitcnt vmcnt(7)
	v_pk_add_f32 v[40:41], v[40:41], v[28:29]
	v_pk_add_f32 v[42:43], v[42:43], v[30:31]
	global_load_dwordx4 v[24:27], v[44:45], off offset:1024
	global_load_dwordx4 v[28:31], v[46:47], off offset:1024
	s_waitcnt vmcnt(8)
	v_pk_add_f32 v[44:45], v[40:41], v[32:33]
	v_pk_add_f32 v[46:47], v[42:43], v[34:35]
	global_load_dwordx4 v[32:35], v[50:51], off offset:1024
	global_load_dwordx4 v[40:43], v[52:53], off offset:1024
	s_waitcnt vmcnt(9)
	v_pk_add_f32 v[50:51], v[44:45], v[36:37]
	v_pk_add_f32 v[52:53], v[46:47], v[38:39]
	global_load_dwordx4 v[36:39], v[54:55], off offset:1024
	global_load_dwordx4 v[44:47], v[64:65], off offset:1024
	s_waitcnt vmcnt(10)
	v_pk_add_f32 v[4:5], v[50:51], v[4:5]
	v_pk_add_f32 v[6:7], v[52:53], v[6:7]
	s_waitcnt vmcnt(9)
	v_pk_add_f32 v[50:51], v[4:5], v[12:13]
	v_pk_add_f32 v[52:53], v[6:7], v[14:15]
	global_load_dwordx4 v[4:7], v0, s[8:9]
	global_load_dwordx4 v[12:15], v0, s[10:11]
	s_waitcnt vmcnt(10)
	v_pk_add_f32 v[16:17], v[50:51], v[16:17]
	v_pk_add_f32 v[18:19], v[52:53], v[18:19]
	s_waitcnt vmcnt(9)
	v_pk_add_f32 v[8:9], v[56:57], v[8:9]
	s_waitcnt vmcnt(8)
	v_pk_add_f32 v[50:51], v[16:17], v[20:21]
	v_pk_add_f32 v[52:53], v[18:19], v[22:23]
	global_load_dwordx4 v[16:19], v0, s[8:9] offset:1024
	global_load_dwordx4 v[20:23], v0, s[10:11] offset:1024
	v_pk_add_f32 v[10:11], v[58:59], v[10:11]
	s_waitcnt vmcnt(9)
	v_pk_add_f32 v[8:9], v[8:9], v[24:25]
	v_add_f32_e32 v24, 0, v50
	s_waitcnt vmcnt(8)
	v_pk_add_f32 v[8:9], v[8:9], v[28:29]
	v_pk_add_f32 v[10:11], v[10:11], v[26:27]
	s_waitcnt vmcnt(7)
	v_pk_add_f32 v[8:9], v[8:9], v[32:33]
	v_add_f32_e32 v24, v24, v51
	s_waitcnt vmcnt(6)
	v_pk_add_f32 v[8:9], v[8:9], v[40:41]
	v_pk_add_f32 v[10:11], v[10:11], v[30:31]
	v_add_f32_e32 v24, v24, v52
	s_waitcnt vmcnt(5)
	v_pk_add_f32 v[8:9], v[8:9], v[36:37]
	v_pk_add_f32 v[10:11], v[10:11], v[34:35]
	v_add_f32_e32 v24, v24, v53
	s_waitcnt vmcnt(4)
	v_pk_add_f32 v[8:9], v[8:9], v[44:45]
	v_pk_add_f32 v[10:11], v[10:11], v[42:43]
	v_add_f32_e32 v24, v24, v8
	v_pk_add_f32 v[10:11], v[10:11], v[38:39]
	v_add_f32_e32 v24, v24, v9
	v_pk_add_f32 v[10:11], v[10:11], v[46:47]
	s_nop 0
	v_add_f32_e32 v24, v24, v10
	v_add_f32_e32 v24, v24, v11
	s_nop 1
	v_add_f32_dpp v24, v24, v24 quad_perm:[1,0,3,2] row_mask:0xf bank_mask:0xf bound_ctrl:1
	s_nop 1
	v_add_f32_dpp v24, v24, v24 quad_perm:[2,3,0,1] row_mask:0xf bank_mask:0xf bound_ctrl:1
	s_nop 1
	v_add_f32_dpp v24, v24, v24 row_half_mirror row_mask:0xf bank_mask:0xf bound_ctrl:1
	s_nop 1
	v_add_f32_dpp v24, v24, v24 row_mirror row_mask:0xf bank_mask:0xf bound_ctrl:1
	s_nop 0
	v_readlane_b32 s8, v24, 16
	v_readlane_b32 s9, v24, 48
	v_readlane_b32 s0, v24, 0
	v_readlane_b32 s1, v24, 32
	v_mov_b32_e32 v24, s8
	v_mov_b32_e32 v25, s9
	v_pk_add_f32 v[24:25], s[0:1], v[24:25]
	s_nop 0
	v_add_f32_e32 v24, v24, v25
	v_mul_f32_e32 v24, 0x3b000000, v24
	v_pk_add_f32 v[26:27], v[50:51], v[24:25] op_sel_hi:[1,0] neg_lo:[0,1] neg_hi:[0,1]
	v_pk_add_f32 v[30:31], v[52:53], v[24:25] op_sel_hi:[1,0] neg_lo:[0,1] neg_hi:[0,1]
	v_pk_mul_f32 v[28:29], v[26:27], v[26:27]
	v_pk_mul_f32 v[32:33], v[30:31], v[30:31]
	v_add_f32_e32 v28, v28, v29
	v_pk_add_f32 v[8:9], v[8:9], v[24:25] op_sel_hi:[1,0] neg_lo:[0,1] neg_hi:[0,1]
	v_add_f32_e32 v28, v28, v32
	v_pk_mul_f32 v[34:35], v[8:9], v[8:9]
	v_add_f32_e32 v28, v28, v33
	v_pk_add_f32 v[10:11], v[10:11], v[24:25] op_sel_hi:[1,0] neg_lo:[0,1] neg_hi:[0,1]
	v_add_f32_e32 v28, v28, v34
	v_pk_mul_f32 v[24:25], v[10:11], v[10:11]
	v_add_f32_e32 v28, v28, v35
	v_add_f32_e32 v24, v28, v24
	v_add_f32_e32 v24, v24, v25
	s_waitcnt vmcnt(3)
	v_pk_mul_f32 v[4:5], v[4:5], v[26:27]
	v_add_f32_dpp v24, v24, v24 quad_perm:[1,0,3,2] row_mask:0xf bank_mask:0xf bound_ctrl:1
	v_pk_mul_f32 v[6:7], v[6:7], v[30:31]
	s_waitcnt vmcnt(1)
	v_pk_mul_f32 v[8:9], v[16:17], v[8:9]
	v_add_f32_dpp v24, v24, v24 quad_perm:[2,3,0,1] row_mask:0xf bank_mask:0xf bound_ctrl:1
	v_pk_mul_f32 v[10:11], v[18:19], v[10:11]
	s_nop 0
	v_add_f32_dpp v24, v24, v24 row_half_mirror row_mask:0xf bank_mask:0xf bound_ctrl:1
	s_nop 1
	v_add_f32_dpp v24, v24, v24 row_mirror row_mask:0xf bank_mask:0xf bound_ctrl:1
	s_nop 0
	v_readlane_b32 s8, v24, 16
	v_readlane_b32 s9, v24, 48
	v_readlane_b32 s0, v24, 0
	v_readlane_b32 s1, v24, 32
	v_mov_b32_e32 v24, s8
	v_mov_b32_e32 v25, s9
	v_pk_add_f32 v[24:25], s[0:1], v[24:25]
	s_mov_b32 s0, 0xf800000
	v_add_f32_e32 v24, v24, v25
	v_mov_b32_e32 v25, 0x3727c5ac
	v_fmac_f32_e32 v25, 0x3b000000, v24
	v_mul_f32_e32 v24, 0x4f800000, v25
	v_cmp_gt_f32_e32 vcc, s0, v25
	s_nop 1
	v_cndmask_b32_e32 v24, v25, v24, vcc
	v_sqrt_f32_e32 v25, v24
	s_nop 0
	v_add_u32_e32 v28, -1, v25
	v_fma_f32 v29, -v28, v25, v24
	v_cmp_ge_f32_e64 s[0:1], 0, v29
	v_add_u32_e32 v29, 1, v25
	s_nop 0
	v_cndmask_b32_e64 v28, v25, v28, s[0:1]
	v_fma_f32 v25, -v29, v25, v24
	v_cmp_lt_f32_e64 s[0:1], 0, v25
	s_nop 1
	v_cndmask_b32_e64 v25, v28, v29, s[0:1]
	v_mul_f32_e32 v28, 0x37800000, v25
	v_cndmask_b32_e32 v25, v25, v28, vcc
	v_mov_b32_e32 v28, 0x260
	v_cmp_class_f32_e32 vcc, v24, v28
	s_nop 1
	v_cndmask_b32_e32 v28, v25, v24, vcc
	v_div_scale_f32 v29, s[0:1], v28, v28, 1.0
	v_rcp_f32_e32 v32, v29
	v_lshl_add_u64 v[24:25], s[4:5], 0, v[48:49]
	v_lshl_add_u64 v[24:25], v[24:25], 0, v[0:1]
	s_mov_b32 s0, 0x43000000
	v_fma_f32 v0, -v29, v32, 1.0
	v_fmac_f32_e32 v32, v0, v32
	v_div_scale_f32 v0, vcc, 1.0, v28, 1.0
	v_mul_f32_e32 v33, v0, v32
	v_fma_f32 v34, -v29, v33, v0
	v_fmac_f32_e32 v33, v34, v32
	v_fma_f32 v0, -v29, v33, v0
	v_div_fmas_f32 v0, v0, v32, v33
	v_div_fixup_f32 v0, v0, v28, 1.0
	v_pk_fma_f32 v[4:5], v[0:1], v[4:5], v[12:13] op_sel_hi:[0,1,1]
	v_pk_fma_f32 v[6:7], v[0:1], v[6:7], v[14:15] op_sel_hi:[0,1,1]
	s_waitcnt vmcnt(0)
	v_pk_fma_f32 v[8:9], v[0:1], v[8:9], v[20:21] op_sel_hi:[0,1,1]
	v_fma_mixlo_f16 v12, v4, s0, 0
	v_pk_fma_f32 v[10:11], v[0:1], v[10:11], v[22:23] op_sel_hi:[0,1,1]
	global_store_dwordx4 v[24:25], v[4:7], off sc1
	global_store_dwordx4 v[24:25], v[8:11], off offset:1024 sc1
	v_mul_f32_e32 v0, 0x43000000, v4
	v_fma_mixlo_f16 v4, v4, s0, -v12 op_sel_hi:[0,0,1]
	v_fma_mixlo_f16 v12, v8, s0, 0
	v_mul_f32_e32 v13, 0x43000000, v8
	v_fma_mixlo_f16 v8, v8, s0, -v12 op_sel_hi:[0,0,1]
	v_mul_f32_e32 v12, 0x43000000, v5
	v_fma_mixlo_f16 v14, v5, s0, 0
	v_cvt_pk_f16_f32 v12, v0, v12
	v_mul_f32_e32 v0, 0x43000000, v9
	v_pk_mul_f32 v[16:17], v[6:7], s[0:1] op_sel_hi:[1,0]
	v_fma_mixhi_f16 v4, v5, s0, -v14 op_sel_hi:[0,0,1]
	v_cvt_pk_f16_f32 v14, v13, v0
	v_cvt_pk_f16_f32 v13, v16, v17
	v_pk_mul_f32 v[18:19], v[10:11], s[0:1] op_sel_hi:[1,0]
	v_cvt_f32_f16_e32 v16, v13
	v_cvt_f32_f16_sdwa v17, v13 dst_sel:DWORD dst_unused:UNUSED_PAD src0_sel:WORD_1
	v_cvt_pk_f16_f32 v15, v18, v19
	v_cvt_f32_f16_e32 v18, v15
	v_cvt_f32_f16_sdwa v19, v15 dst_sel:DWORD dst_unused:UNUSED_PAD src0_sel:WORD_1
	v_fma_mixlo_f16 v5, v9, s0, 0
	v_pk_fma_f32 v[6:7], v[6:7], s[0:1], v[16:17] op_sel_hi:[1,0,1] neg_lo:[0,0,1] neg_hi:[0,0,1]
	v_fma_mixhi_f16 v8, v9, s0, -v5 op_sel_hi:[0,0,1]
	v_cvt_pk_f16_f32 v5, v6, v7
	v_pk_fma_f32 v[6:7], v[10:11], s[0:1], v[18:19] op_sel_hi:[1,0,1] neg_lo:[0,0,1] neg_hi:[0,0,1]
	v_lshlrev_b32_e32 v0, 1, v66
	v_cvt_pk_f16_f32 v9, v6, v7
	v_lshl_add_u64 v[6:7], s[6:7], 0, v[2:3]
	v_lshl_add_u64 v[2:3], s[2:3], 0, v[2:3]
	v_lshl_add_u64 v[6:7], v[6:7], 0, v[0:1]
	v_lshl_add_u64 v[0:1], v[2:3], 0, v[0:1]
	v_mbcnt_lo_u32_b32 v20, -1, 0
	v_mbcnt_hi_u32_b32 v20, -1, v20
	v_and_b32_e32 v20, 1, v20
	v_cmp_eq_u32_e32 vcc, 1, v20
	v_mul_u32_u24_e32 v22, 0x1f8, v20
	v_mov_b32_e32 v23, 0
	s_nop 1
	v_mov_b32_dpp v24, v12 quad_perm:[1,0,3,2] row_mask:0xf bank_mask:0xf
	v_mov_b32_dpp v25, v13 quad_perm:[1,0,3,2] row_mask:0xf bank_mask:0xf
	v_mov_b32_dpp v26, v14 quad_perm:[1,0,3,2] row_mask:0xf bank_mask:0xf
	v_mov_b32_dpp v27, v15 quad_perm:[1,0,3,2] row_mask:0xf bank_mask:0xf
	s_nop 1
	v_cndmask_b32_e32 v28, v12, v26, vcc
	v_cndmask_b32_e32 v29, v13, v27, vcc
	v_cndmask_b32_e32 v30, v24, v14, vcc
	v_cndmask_b32_e32 v31, v25, v15, vcc
	v_lshl_add_u64 v[32:33], v[6:7], 0, v[22:23]
	global_store_dwordx4 v[32:33], v[28:31], off sc1
	s_nop 1
	v_mov_b32_dpp v24, v4 quad_perm:[1,0,3,2] row_mask:0xf bank_mask:0xf
	v_mov_b32_dpp v25, v5 quad_perm:[1,0,3,2] row_mask:0xf bank_mask:0xf
	v_mov_b32_dpp v26, v8 quad_perm:[1,0,3,2] row_mask:0xf bank_mask:0xf
	v_mov_b32_dpp v27, v9 quad_perm:[1,0,3,2] row_mask:0xf bank_mask:0xf
	s_nop 1
	v_cndmask_b32_e32 v28, v4, v26, vcc
	v_cndmask_b32_e32 v29, v5, v27, vcc
	v_cndmask_b32_e32 v30, v24, v8, vcc
	v_cndmask_b32_e32 v31, v25, v9, vcc
	v_lshl_add_u64 v[32:33], v[0:1], 0, v[22:23]
	global_store_dwordx4 v[32:33], v[28:31], off sc1
	s_nop 1
	s_endpgm
	s_endpgm
	s_endpgm
	s_endpgm
	s_endpgm
	s_endpgm
	s_endpgm
	s_endpgm
	s_endpgm
	s_endpgm
	s_endpgm
	s_endpgm
	s_endpgm
	s_endpgm
	s_endpgm
	s_endpgm
	s_endpgm
	s_endpgm
	s_endpgm
	s_endpgm
